# P0 converter stores write-through (sc1) so the P0 seam's L2 write-back has nothing left to flush
# speedup vs baseline: 1.0082x; 1.0003x over previous
; __device__ __forceinline__ void conv_load(const ConvItem& ci, int lane, float (&v)[64]) {
;     const bool okc = ci.srcc >= 0 && (ci.srcc + lane) < ci.ncols;
;     const float* base = ci.W + (okc ? ci.srcc + lane : 0);
;     const int kmax = ci.Ksrc - 1;
; #pragma unroll
;     for (int i = 0; i < 64; ++i) { const int k = ci.k0 + i, kk = k < kmax ? k : kmax; v[i] = __builtin_nontemporal_load(base + (size_t)kk * ci.ldw); }
; #pragma unroll
;     for (int i = 0; i < 64; ++i) v[i] = (okc && (ci.k0 + i) < ci.Ksrc) ? v[i] : 0.f;
.LBB0_30:
	s_cmp_lt_i32 s58, s76
	s_cselect_b64 s[4:5], -1, 0
	s_and_b64 s[4:5], vcc, s[4:5]
	s_cmp_lt_i32 s64, s76
	s_waitcnt vmcnt(62)
	v_cndmask_b32_e64 v21, 0, v21, s[4:5]
	s_cselect_b64 s[4:5], -1, 0
	s_and_b64 s[4:5], vcc, s[4:5]
	s_cmp_lt_i32 s65, s76
	v_cndmask_b32_e64 v20, 0, v20, s[4:5]
	s_cselect_b64 s[4:5], -1, 0
	s_and_b64 s[4:5], vcc, s[4:5]
	s_cmp_lt_i32 s78, s76
	s_waitcnt vmcnt(61)
	v_cndmask_b32_e64 v19, 0, v19, s[4:5]
	s_cselect_b64 s[4:5], -1, 0
	s_and_b64 s[4:5], vcc, s[4:5]
	s_cmp_lt_i32 s79, s76
	s_waitcnt vmcnt(60)
	v_cndmask_b32_e64 v18, 0, v18, s[4:5]
	s_cselect_b64 s[4:5], -1, 0
	s_and_b64 s[4:5], vcc, s[4:5]
	s_cmp_lt_i32 s80, s76
	s_waitcnt vmcnt(59)
	v_cndmask_b32_e64 v17, 0, v17, s[4:5]
	s_cselect_b64 s[4:5], -1, 0
	s_and_b64 s[4:5], vcc, s[4:5]
	s_cmp_lt_i32 s81, s76
	s_waitcnt vmcnt(58)
	v_cndmask_b32_e64 v16, 0, v16, s[4:5]
	s_cselect_b64 s[4:5], -1, 0
	s_and_b64 s[4:5], vcc, s[4:5]
	s_cmp_lt_i32 s82, s76
	s_waitcnt vmcnt(57)
	v_cndmask_b32_e64 v15, 0, v15, s[4:5]
	s_cselect_b64 s[4:5], -1, 0
	s_and_b64 s[4:5], vcc, s[4:5]
	s_cmp_lt_i32 s83, s76
	s_waitcnt vmcnt(56)
	v_cndmask_b32_e64 v8, 0, v8, s[4:5]
	s_cselect_b64 s[4:5], -1, 0
	s_and_b64 s[4:5], vcc, s[4:5]
	s_cmp_lt_i32 s85, s76
	s_waitcnt vmcnt(55)
	v_cndmask_b32_e64 v29, 0, v29, s[4:5]
	s_cselect_b64 s[4:5], -1, 0
	s_and_b64 s[4:5], vcc, s[4:5]
	s_cmp_lt_i32 s86, s76
	s_waitcnt vmcnt(54)
	v_cndmask_b32_e64 v28, 0, v28, s[4:5]
	s_cselect_b64 s[4:5], -1, 0
	s_and_b64 s[4:5], vcc, s[4:5]
	s_cmp_lt_i32 s87, s76
	s_waitcnt vmcnt(53)
	v_cndmask_b32_e64 v27, 0, v27, s[4:5]
	s_cselect_b64 s[4:5], -1, 0
	s_and_b64 s[4:5], vcc, s[4:5]
	s_cmp_lt_i32 s88, s76
	s_waitcnt vmcnt(52)
	v_cndmask_b32_e64 v26, 0, v26, s[4:5]
	s_cselect_b64 s[4:5], -1, 0
	s_and_b64 s[4:5], vcc, s[4:5]
	s_cmp_lt_i32 s89, s76
	s_waitcnt vmcnt(51)
	v_cndmask_b32_e64 v25, 0, v25, s[4:5]
	s_cselect_b64 s[4:5], -1, 0
	s_and_b64 s[4:5], vcc, s[4:5]
	s_cmp_lt_i32 s90, s76
	s_waitcnt vmcnt(50)
	v_cndmask_b32_e64 v24, 0, v24, s[4:5]
	s_cselect_b64 s[4:5], -1, 0
	s_and_b64 s[4:5], vcc, s[4:5]
	s_cmp_lt_i32 s92, s76
	s_waitcnt vmcnt(49)
	v_cndmask_b32_e64 v23, 0, v23, s[4:5]
	s_cselect_b64 s[4:5], -1, 0
	s_and_b64 s[4:5], vcc, s[4:5]
	s_cmp_lt_i32 s93, s76
	s_waitcnt vmcnt(48)
	v_cndmask_b32_e64 v22, 0, v22, s[4:5]
	s_cselect_b64 s[4:5], -1, 0
	s_and_b64 s[4:5], vcc, s[4:5]
	s_cmp_lt_i32 s94, s76
	s_waitcnt vmcnt(47)
	v_cndmask_b32_e64 v37, 0, v37, s[4:5]
	s_cselect_b64 s[4:5], -1, 0
	s_and_b64 s[4:5], vcc, s[4:5]
	s_cmp_lt_i32 s95, s76
	s_waitcnt vmcnt(46)
	v_cndmask_b32_e64 v36, 0, v36, s[4:5]
	s_cselect_b64 s[4:5], -1, 0
	s_and_b64 s[4:5], vcc, s[4:5]
	s_cmp_lt_i32 s50, s76
	s_waitcnt vmcnt(45)
	v_cndmask_b32_e64 v35, 0, v35, s[4:5]
	s_cselect_b64 s[4:5], -1, 0
	s_and_b64 s[4:5], vcc, s[4:5]
	s_cmp_lt_i32 s51, s76
	s_waitcnt vmcnt(44)
	v_cndmask_b32_e64 v34, 0, v34, s[4:5]
	s_cselect_b64 s[4:5], -1, 0
	s_and_b64 s[4:5], vcc, s[4:5]
	s_cmp_lt_i32 s52, s76
	s_waitcnt vmcnt(43)
	v_cndmask_b32_e64 v33, 0, v33, s[4:5]
	s_cselect_b64 s[4:5], -1, 0
	s_and_b64 s[4:5], vcc, s[4:5]
	s_cmp_lt_i32 s53, s76
	s_waitcnt vmcnt(42)
	v_cndmask_b32_e64 v32, 0, v32, s[4:5]
	s_cselect_b64 s[4:5], -1, 0
	s_and_b64 s[4:5], vcc, s[4:5]
	s_cmp_lt_i32 s6, s76
	s_waitcnt vmcnt(41)
	v_cndmask_b32_e64 v31, 0, v31, s[4:5]
	s_cselect_b64 s[4:5], -1, 0
	s_and_b64 s[4:5], vcc, s[4:5]
	s_cmp_lt_i32 s7, s76
	s_waitcnt vmcnt(40)
	v_cndmask_b32_e64 v30, 0, v30, s[4:5]
	s_cselect_b64 s[4:5], -1, 0
	s_and_b64 s[4:5], vcc, s[4:5]
	s_cmp_lt_i32 s8, s76
	s_waitcnt vmcnt(39)
	v_cndmask_b32_e64 v45, 0, v45, s[4:5]
	s_cselect_b64 s[4:5], -1, 0
	s_and_b64 s[4:5], vcc, s[4:5]
	s_cmp_lt_i32 s9, s76
	s_waitcnt vmcnt(38)
	v_cndmask_b32_e64 v44, 0, v44, s[4:5]
	s_cselect_b64 s[4:5], -1, 0
	s_and_b64 s[4:5], vcc, s[4:5]
	s_cmp_lt_i32 s10, s76
	s_waitcnt vmcnt(37)
	v_cndmask_b32_e64 v43, 0, v43, s[4:5]
	s_cselect_b64 s[4:5], -1, 0
	s_and_b64 s[4:5], vcc, s[4:5]
	s_cmp_lt_i32 s11, s76
	s_waitcnt vmcnt(36)
	v_cndmask_b32_e64 v42, 0, v42, s[4:5]
	s_cselect_b64 s[4:5], -1, 0
	s_and_b64 s[4:5], vcc, s[4:5]
	s_cmp_lt_i32 s14, s76
	s_waitcnt vmcnt(35)
	v_cndmask_b32_e64 v41, 0, v41, s[4:5]
	s_cselect_b64 s[4:5], -1, 0
	s_and_b64 s[4:5], vcc, s[4:5]
	s_cmp_lt_i32 s15, s76
	s_waitcnt vmcnt(34)
	v_cndmask_b32_e64 v40, 0, v40, s[4:5]
	s_cselect_b64 s[4:5], -1, 0
	s_and_b64 s[4:5], vcc, s[4:5]
	s_cmp_lt_i32 s16, s76
	s_waitcnt vmcnt(33)
	v_cndmask_b32_e64 v39, 0, v39, s[4:5]
	s_cselect_b64 s[4:5], -1, 0
	s_and_b64 s[4:5], vcc, s[4:5]
	s_cmp_lt_i32 s17, s76
	s_waitcnt vmcnt(32)
	v_cndmask_b32_e64 v38, 0, v38, s[4:5]
	s_cselect_b64 s[4:5], -1, 0
	s_and_b64 s[4:5], vcc, s[4:5]
	s_cmp_lt_i32 s12, s76
	s_waitcnt vmcnt(31)
	v_cndmask_b32_e64 v53, 0, v53, s[4:5]
	s_cselect_b64 s[4:5], -1, 0
	s_and_b64 s[4:5], vcc, s[4:5]
	s_cmp_lt_i32 s13, s76
	s_waitcnt vmcnt(30)
	v_cndmask_b32_e64 v52, 0, v52, s[4:5]
	s_cselect_b64 s[4:5], -1, 0
	s_and_b64 s[4:5], vcc, s[4:5]
	s_cmp_lt_i32 s20, s76
	s_waitcnt vmcnt(29)
	v_cndmask_b32_e64 v51, 0, v51, s[4:5]
	s_cselect_b64 s[4:5], -1, 0
	s_and_b64 s[4:5], vcc, s[4:5]
	s_cmp_lt_i32 s21, s76
	s_waitcnt vmcnt(28)
	v_cndmask_b32_e64 v50, 0, v50, s[4:5]
	s_cselect_b64 s[4:5], -1, 0
	s_and_b64 s[4:5], vcc, s[4:5]
	s_cmp_lt_i32 s24, s76
	s_waitcnt vmcnt(27)
	v_cndmask_b32_e64 v49, 0, v49, s[4:5]
	s_cselect_b64 s[4:5], -1, 0
	s_and_b64 s[4:5], vcc, s[4:5]
	s_cmp_lt_i32 s25, s76
	s_waitcnt vmcnt(26)
	v_cndmask_b32_e64 v48, 0, v48, s[4:5]
	s_cselect_b64 s[4:5], -1, 0
	s_and_b64 s[4:5], vcc, s[4:5]
	s_cmp_lt_i32 s26, s76
	s_waitcnt vmcnt(25)
	v_cndmask_b32_e64 v47, 0, v47, s[4:5]
	s_cselect_b64 s[4:5], -1, 0
	s_and_b64 s[4:5], vcc, s[4:5]
	s_cmp_lt_i32 s27, s76
	s_waitcnt vmcnt(24)
; #define LAS __attribute__((address_space(3)))
; #define LDS_WAIT() asm volatile("s_waitcnt lgkmcnt(0)" ::: "memory")
; __device__ __forceinline__ void conv_load(const ConvItem& ci, int lane, float (&v)[64]) {
;     ...
;     for (int i = 0; i < 64; ++i) v[i] = (okc && (ci.k0 + i) < ci.Ksrc) ? v[i] : 0.f;
; }
; __device__ __forceinline__ void conv_store(const ConvItem& ci, LAS float* scr, int lane, const float (&v)[64]) {
;     const int c = lane & 7;
;     f32x4 s0 = {1.f, 1.f, 1.f, 1.f}, s1 = s0;
;     if (ci.ks) { const int kb = ci.k0 + 8 * c < ci.Ksrc - 8 ? ci.k0 + 8 * c : ci.Ksrc - 8; s0 = *(const f32x4*)(ci.ks + kb); s1 = *(const f32x4*)(ci.ks + kb + 4); }
; #pragma unroll
;     for (int i = 0; i < 64; ++i) scr[i * 65 + lane] = v[i];
;     LDS_WAIT(); asm volatile("" ::: "memory");
; #pragma unroll
;     for (int j = 0; j < 8; ++j) { const int n = (lane >> 3) + 8 * j; const LAS float* s = scr + (8 * c) * 65 + n;
	v_cndmask_b32_e64 v46, 0, v46, s[4:5]
	s_cselect_b64 s[4:5], -1, 0
	s_and_b64 s[4:5], vcc, s[4:5]
	s_cmp_lt_i32 s18, s76
	s_waitcnt vmcnt(23)
	v_cndmask_b32_e64 v61, 0, v61, s[4:5]
	s_cselect_b64 s[4:5], -1, 0
	s_and_b64 s[4:5], vcc, s[4:5]
	s_cmp_lt_i32 s19, s76
	s_waitcnt vmcnt(22)
	v_cndmask_b32_e64 v60, 0, v60, s[4:5]
	s_cselect_b64 s[4:5], -1, 0
	s_and_b64 s[4:5], vcc, s[4:5]
	s_cmp_lt_i32 s28, s76
	s_waitcnt vmcnt(21)
	v_cndmask_b32_e64 v59, 0, v59, s[4:5]
	s_cselect_b64 s[4:5], -1, 0
	s_and_b64 s[4:5], vcc, s[4:5]
	s_cmp_lt_i32 s29, s76
	s_waitcnt vmcnt(20)
	v_cndmask_b32_e64 v58, 0, v58, s[4:5]
	s_cselect_b64 s[4:5], -1, 0
	s_and_b64 s[4:5], vcc, s[4:5]
	s_cmp_lt_i32 s22, s76
	s_waitcnt vmcnt(19)
	v_cndmask_b32_e64 v57, 0, v57, s[4:5]
	s_cselect_b64 s[4:5], -1, 0
	s_and_b64 s[4:5], vcc, s[4:5]
	s_cmp_lt_i32 s23, s76
	s_waitcnt vmcnt(18)
	v_cndmask_b32_e64 v56, 0, v56, s[4:5]
	s_cselect_b64 s[4:5], -1, 0
	s_and_b64 s[4:5], vcc, s[4:5]
	s_cmp_lt_i32 s30, s76
	s_waitcnt vmcnt(17)
	v_cndmask_b32_e64 v55, 0, v55, s[4:5]
	s_cselect_b64 s[4:5], -1, 0
	s_and_b64 s[4:5], vcc, s[4:5]
	s_cmp_lt_i32 s31, s76
	s_waitcnt vmcnt(16)
	v_cndmask_b32_e64 v54, 0, v54, s[4:5]
	s_cselect_b64 s[4:5], -1, 0
	s_and_b64 s[4:5], vcc, s[4:5]
	s_cmp_lt_i32 s36, s76
	s_waitcnt vmcnt(15)
	v_cndmask_b32_e64 v70, 0, v70, s[4:5]
	s_cselect_b64 s[4:5], -1, 0
	s_and_b64 s[4:5], vcc, s[4:5]
	s_cmp_lt_i32 s37, s76
	s_waitcnt vmcnt(14)
	v_cndmask_b32_e64 v69, 0, v69, s[4:5]
	s_cselect_b64 s[4:5], -1, 0
	s_and_b64 s[4:5], vcc, s[4:5]
	s_cmp_lt_i32 s38, s76
	s_waitcnt vmcnt(13)
	v_cndmask_b32_e64 v68, 0, v68, s[4:5]
	s_cselect_b64 s[4:5], -1, 0
	s_and_b64 s[4:5], vcc, s[4:5]
	s_cmp_lt_i32 s39, s76
	s_waitcnt vmcnt(12)
	v_cndmask_b32_e64 v67, 0, v67, s[4:5]
	s_cselect_b64 s[4:5], -1, 0
	s_and_b64 s[4:5], vcc, s[4:5]
	s_cmp_lt_i32 s34, s76
	s_waitcnt vmcnt(11)
	v_cndmask_b32_e64 v66, 0, v66, s[4:5]
	s_cselect_b64 s[4:5], -1, 0
	s_and_b64 s[4:5], vcc, s[4:5]
	s_cmp_lt_i32 s35, s76
	s_waitcnt vmcnt(10)
	v_cndmask_b32_e64 v64, 0, v64, s[4:5]
	s_cselect_b64 s[4:5], -1, 0
	s_and_b64 s[4:5], vcc, s[4:5]
	s_cmp_lt_i32 s42, s76
	s_waitcnt vmcnt(9)
	v_cndmask_b32_e64 v63, 0, v63, s[4:5]
	s_cselect_b64 s[4:5], -1, 0
	s_and_b64 s[4:5], vcc, s[4:5]
	s_cmp_lt_i32 s43, s76
	s_waitcnt vmcnt(8)
	v_cndmask_b32_e64 v62, 0, v62, s[4:5]
	s_cselect_b64 s[4:5], -1, 0
	s_and_b64 s[4:5], vcc, s[4:5]
	s_cmp_lt_i32 s54, s76
	s_waitcnt vmcnt(7)
	v_cndmask_b32_e64 v65, 0, v65, s[4:5]
	s_cselect_b64 s[4:5], -1, 0
	s_and_b64 s[4:5], vcc, s[4:5]
	s_cmp_lt_i32 s55, s76
	s_waitcnt vmcnt(6)
	v_cndmask_b32_e64 v74, 0, v74, s[4:5]
	s_cselect_b64 s[4:5], -1, 0
	s_and_b64 s[4:5], vcc, s[4:5]
	s_cmp_lt_i32 s46, s76
	ds_write2_b32 v12, v21, v20 offset1:65
	ds_write2_b32 v12, v19, v18 offset0:130 offset1:195
	v_add_u32_e32 v18, 0x400, v12
	s_waitcnt vmcnt(5)
	v_cndmask_b32_e64 v73, 0, v73, s[4:5]
	s_cselect_b64 s[4:5], -1, 0
	ds_write2_b32 v18, v17, v16 offset0:4 offset1:69
	ds_write2_b32 v18, v15, v8 offset0:134 offset1:199
	v_add_u32_e32 v8, 0x800, v12
	s_and_b64 s[4:5], vcc, s[4:5]
	ds_write2_b32 v8, v29, v28 offset0:8 offset1:73
	ds_write2_b32 v8, v27, v26 offset0:138 offset1:203
	v_add_u32_e32 v8, 0xc00, v12
	s_cmp_lt_i32 s47, s76
	ds_write2_b32 v8, v25, v24 offset0:12 offset1:77
	ds_write2_b32 v8, v23, v22 offset0:142 offset1:207
	v_add_u32_e32 v8, 0x1000, v12
	s_waitcnt vmcnt(4)
	v_cndmask_b32_e64 v72, 0, v72, s[4:5]
	s_cselect_b64 s[4:5], -1, 0
	ds_write2_b32 v8, v37, v36 offset0:16 offset1:81
	ds_write2_b32 v8, v35, v34 offset0:146 offset1:211
	v_add_u32_e32 v8, 0x1400, v12
	s_and_b64 s[4:5], vcc, s[4:5]
	ds_write2_b32 v8, v33, v32 offset0:20 offset1:85
	ds_write2_b32 v8, v31, v30 offset0:150 offset1:215
	v_add_u32_e32 v8, 0x1800, v12
	s_cmp_lt_i32 s48, s76
	ds_write2_b32 v8, v45, v44 offset0:24 offset1:89
	ds_write2_b32 v8, v43, v42 offset0:154 offset1:219
	v_add_u32_e32 v8, 0x1c00, v12
	s_waitcnt vmcnt(3)
	v_cndmask_b32_e64 v71, 0, v71, s[4:5]
	s_cselect_b64 s[4:5], -1, 0
	ds_write2_b32 v8, v41, v40 offset0:28 offset1:93
	ds_write2_b32 v8, v39, v38 offset0:158 offset1:223
	v_add_u32_e32 v8, 0x2000, v12
	s_and_b64 s[4:5], vcc, s[4:5]
	ds_write2_b32 v8, v53, v52 offset0:32 offset1:97
	ds_write2_b32 v8, v51, v50 offset0:162 offset1:227
	v_add_u32_e32 v8, 0x2400, v12
	s_cmp_lt_i32 s49, s76
	ds_write2_b32 v8, v49, v48 offset0:36 offset1:101
	ds_write2_b32 v8, v47, v46 offset0:166 offset1:231
	v_add_u32_e32 v8, 0x2800, v12
	s_waitcnt vmcnt(2)
	v_cndmask_b32_e64 v77, 0, v77, s[4:5]
	s_cselect_b64 s[4:5], -1, 0
	ds_write2_b32 v8, v61, v60 offset0:40 offset1:105
	ds_write2_b32 v8, v59, v58 offset0:170 offset1:235
	v_add_u32_e32 v8, 0x2c00, v12
	s_and_b64 s[4:5], vcc, s[4:5]
	ds_write2_b32 v8, v57, v56 offset0:44 offset1:109
	ds_write2_b32 v8, v55, v54 offset0:174 offset1:239
	v_add_u32_e32 v8, 0x3000, v12
	s_cmp_lt_i32 s44, s76
	ds_write2_b32 v8, v70, v69 offset0:48 offset1:113
	ds_write2_b32 v8, v68, v67 offset0:178 offset1:243
	v_add_u32_e32 v8, 0x3400, v12
	s_waitcnt vmcnt(1)
	v_cndmask_b32_e64 v76, 0, v76, s[4:5]
	s_cselect_b64 s[4:5], -1, 0
	ds_write2_b32 v8, v66, v64 offset0:52 offset1:117
	ds_write2_b32 v8, v63, v62 offset0:182 offset1:247
	v_add_u32_e32 v8, 0x3800, v12
	s_and_b64 vcc, vcc, s[4:5]
	ds_write2_b32 v8, v65, v74 offset0:56 offset1:121
	ds_write2_b32 v8, v73, v72 offset0:186 offset1:251
	v_add_u32_e32 v8, 0x3c00, v12
	s_waitcnt vmcnt(0)
	v_cndmask_b32_e32 v75, 0, v75, vcc
	ds_write2_b32 v8, v71, v77 offset0:60 offset1:125
	ds_write2_b32 v8, v76, v75 offset0:190 offset1:255
	s_waitcnt lgkmcnt(0)
	ds_read2_b32 v[16:17], v14 offset1:65
	v_add_u32_e32 v24, s59, v13
	v_mul_lo_u32 v22, s57, v24
	s_ashr_i32 s59, s58, 31
	v_readlane_b32 s76, v254, 31
	s_waitcnt lgkmcnt(0)
; __device__ __forceinline__ unsigned cvt_pk_bf16(float lo, float hi) { unsigned r; asm volatile("v_cvt_pk_bf16_f32 %0, %1, %2" : "=v"(r) : "v"(lo), "v"(hi)); return r; }
; #define LAS __attribute__((address_space(3)))
; __device__ __forceinline__ void conv_store(const ConvItem& ci, LAS float* scr, int lane, const float (&v)[64]) {
;     ...
;     for (int j = 0; j < 8; ++j) { const int n = (lane >> 3) + 8 * j; const LAS float* s = scr + (8 * c) * 65 + n;
;         v4u o; o.x = cvt_pk_bf16(s[0 * 65] * s0[0], s[1 * 65] * s0[1]); o.y = cvt_pk_bf16(s[2 * 65] * s0[2], s[3 * 65] * s0[3]); o.z = cvt_pk_bf16(s[4 * 65] * s1[0], s[5 * 65] * s1[1]); o.w = cvt_pk_bf16(s[6 * 65] * s1[2], s[7 * 65] * s1[3]);
;         *(v4u*)(ci.dst + (size_t)(ci.drow0 + n) * ci.ldd + ci.k0 + 8 * c) = o; }
	v_mul_f32_e32 v8, v4, v16
	v_mul_f32_e32 v15, v5, v17
	v_cvt_pk_bf16_f32 v16, v8, v15
	ds_read2_b32 v[18:19], v14 offset0:130 offset1:195
	s_add_i32 s3, s3, s33
	s_add_i32 s66, s66, s67
	s_add_i32 s68, s68, s69
	s_add_i32 s70, s70, s71
	s_waitcnt lgkmcnt(0)
	v_mul_f32_e32 v15, v7, v19
	v_mul_f32_e32 v8, v6, v18
	v_cvt_pk_bf16_f32 v17, v8, v15
	v_add_u32_e32 v15, 0x400, v14
	ds_read2_b32 v[18:19], v15 offset0:4 offset1:69
	s_add_i32 s72, s72, s73
	s_add_i32 s74, s74, s75
	v_readlane_b32 s78, v254, 33
	v_readlane_b32 s79, v254, 34
	s_waitcnt lgkmcnt(0)
	v_mul_f32_e32 v8, v0, v18
	v_mul_f32_e32 v18, v1, v19
	v_cvt_pk_bf16_f32 v18, v8, v18
	ds_read2_b32 v[20:21], v15 offset0:134 offset1:199
	v_readlane_b32 s80, v255, 21
	v_readlane_b32 s77, v254, 32
	s_movk_i32 s78, 0x1580
	v_readlane_b32 s82, v255, 23
	s_waitcnt lgkmcnt(0)
	v_mul_f32_e32 v8, v2, v20
	v_mul_f32_e32 v19, v3, v21
	v_cvt_pk_bf16_f32 v19, v8, v19
	v_ashrrev_i32_e32 v8, 31, v24
	v_mul_lo_u32 v8, s56, v8
	v_mad_u64_u32 v[20:21], s[4:5], s56, v24, 0
	v_add3_u32 v21, v21, v8, v22
	ds_read2_b32 v[22:23], v14 offset0:8 offset1:73
	v_lshl_add_u64 v[20:21], v[20:21], 1, s[60:61]
	s_lshl_b64 s[4:5], s[58:59], 1
	v_lshl_add_u64 v[20:21], v[20:21], 0, s[4:5]
	v_lshlrev_b32_e32 v8, 1, v10
	v_lshl_add_u64 v[20:21], v[20:21], 0, v[8:9]
	global_store_dwordx4 v[20:21], v[16:19], off sc1
	s_cmp_lt_i32 s3, s99
	v_readlane_b32 s83, v255, 24
	s_waitcnt lgkmcnt(0)
	v_mul_f32_e32 v16, v4, v22
	v_mul_f32_e32 v17, v5, v23
	v_cvt_pk_bf16_f32 v16, v16, v17
	ds_read2_b32 v[18:19], v14 offset0:138 offset1:203
	s_mov_b32 s79, 0x3f22f983
	s_mov_b32 s85, 0xbfc90fda
	s_brev_b32 s86, 1
	s_movk_i32 s87, 0x1f8
	s_waitcnt lgkmcnt(0)
	v_mul_f32_e32 v17, v6, v18
	v_mul_f32_e32 v18, v7, v19
	v_cvt_pk_bf16_f32 v17, v17, v18
	ds_read2_b32 v[18:19], v15 offset0:12 offset1:77
	s_mov_b64 s[88:89], 0x80
	s_mov_b64 s[92:93], 0x4000
	s_mov_b64 s[94:95], 0x4800
	v_readlane_b32 s81, v255, 22
	s_waitcnt lgkmcnt(0)
	v_mul_f32_e32 v18, v0, v18
	v_mul_f32_e32 v19, v1, v19
	v_cvt_pk_bf16_f32 v18, v18, v19
	ds_read2_b32 v[20:21], v15 offset0:142 offset1:207
	s_waitcnt lgkmcnt(0)
	v_mul_f32_e32 v19, v2, v20
	v_mul_f32_e32 v20, v3, v21
	v_cvt_pk_bf16_f32 v19, v19, v20
	v_add_u32_e32 v20, 8, v24
	v_ashrrev_i32_e32 v21, 31, v20
	v_mul_lo_u32 v22, s56, v21
	v_mul_lo_u32 v23, s57, v20
	v_mad_u64_u32 v[20:21], s[6:7], s56, v20, 0
	v_add3_u32 v21, v21, v22, v23
	ds_read2_b32 v[22:23], v14 offset0:16 offset1:81
	v_lshl_add_u64 v[20:21], v[20:21], 1, s[60:61]
	v_lshl_add_u64 v[20:21], v[20:21], 0, s[4:5]
	v_lshl_add_u64 v[20:21], v[20:21], 0, v[8:9]
	global_store_dwordx4 v[20:21], v[16:19], off sc1
	s_waitcnt lgkmcnt(0)
	s_nop 0
	v_mul_f32_e32 v16, v4, v22
	v_mul_f32_e32 v17, v5, v23
	v_cvt_pk_bf16_f32 v16, v16, v17
	ds_read2_b32 v[18:19], v14 offset0:146 offset1:211
	s_waitcnt lgkmcnt(0)
	v_mul_f32_e32 v17, v6, v18
	v_mul_f32_e32 v18, v7, v19
	v_cvt_pk_bf16_f32 v17, v17, v18
	ds_read2_b32 v[18:19], v15 offset0:20 offset1:85
	s_waitcnt lgkmcnt(0)
	v_mul_f32_e32 v18, v0, v18
	v_mul_f32_e32 v19, v1, v19
	v_cvt_pk_bf16_f32 v18, v18, v19
	ds_read2_b32 v[20:21], v15 offset0:150 offset1:215
	s_waitcnt lgkmcnt(0)
	v_mul_f32_e32 v19, v2, v20
	v_mul_f32_e32 v20, v3, v21
	v_cvt_pk_bf16_f32 v19, v19, v20
	v_add_u32_e32 v20, 16, v24
	v_ashrrev_i32_e32 v21, 31, v20
	v_mul_lo_u32 v22, s56, v21
	v_mul_lo_u32 v23, s57, v20
	v_mad_u64_u32 v[20:21], s[6:7], s56, v20, 0
	v_add3_u32 v21, v21, v22, v23
	ds_read2_b32 v[22:23], v14 offset0:24 offset1:89
	v_lshl_add_u64 v[20:21], v[20:21], 1, s[60:61]
	v_lshl_add_u64 v[20:21], v[20:21], 0, s[4:5]
	v_lshl_add_u64 v[20:21], v[20:21], 0, v[8:9]
	global_store_dwordx4 v[20:21], v[16:19], off sc1
	s_waitcnt lgkmcnt(0)
	s_nop 0
	v_mul_f32_e32 v16, v4, v22
	v_mul_f32_e32 v17, v5, v23
	v_cvt_pk_bf16_f32 v16, v16, v17
	ds_read2_b32 v[18:19], v14 offset0:154 offset1:219
	s_waitcnt lgkmcnt(0)
	v_mul_f32_e32 v17, v6, v18
	v_mul_f32_e32 v18, v7, v19
	v_cvt_pk_bf16_f32 v17, v17, v18
	ds_read2_b32 v[18:19], v15 offset0:28 offset1:93
	s_waitcnt lgkmcnt(0)
	v_mul_f32_e32 v18, v0, v18
	v_mul_f32_e32 v19, v1, v19
	v_cvt_pk_bf16_f32 v18, v18, v19
	ds_read2_b32 v[20:21], v15 offset0:158 offset1:223
	s_waitcnt lgkmcnt(0)
; __device__ __forceinline__ unsigned cvt_pk_bf16(float lo, float hi) { unsigned r; asm volatile("v_cvt_pk_bf16_f32 %0, %1, %2" : "=v"(r) : "v"(lo), "v"(hi)); return r; }
; #define LAS __attribute__((address_space(3)))
; __device__ __forceinline__ void conv_store(const ConvItem& ci, LAS float* scr, int lane, const float (&v)[64]) {
;     ...
;     for (int j = 0; j < 8; ++j) { const int n = (lane >> 3) + 8 * j; const LAS float* s = scr + (8 * c) * 65 + n;
;         v4u o; o.x = cvt_pk_bf16(s[0 * 65] * s0[0], s[1 * 65] * s0[1]); o.y = cvt_pk_bf16(s[2 * 65] * s0[2], s[3 * 65] * s0[3]); o.z = cvt_pk_bf16(s[4 * 65] * s1[0], s[5 * 65] * s1[1]); o.w = cvt_pk_bf16(s[6 * 65] * s1[2], s[7 * 65] * s1[3]);
;         *(v4u*)(ci.dst + (size_t)(ci.drow0 + n) * ci.ldd + ci.k0 + 8 * c) = o; }
	v_mul_f32_e32 v19, v2, v20
	v_mul_f32_e32 v20, v3, v21
	v_cvt_pk_bf16_f32 v19, v19, v20
	v_add_u32_e32 v20, 24, v24
	v_ashrrev_i32_e32 v21, 31, v20
	v_mul_lo_u32 v22, s56, v21
	v_mul_lo_u32 v23, s57, v20
	v_mad_u64_u32 v[20:21], s[6:7], s56, v20, 0
	v_add3_u32 v21, v21, v22, v23
	ds_read2_b32 v[22:23], v14 offset0:32 offset1:97
	v_lshl_add_u64 v[20:21], v[20:21], 1, s[60:61]
	v_lshl_add_u64 v[20:21], v[20:21], 0, s[4:5]
	v_lshl_add_u64 v[20:21], v[20:21], 0, v[8:9]
	global_store_dwordx4 v[20:21], v[16:19], off sc1
	s_waitcnt lgkmcnt(0)
	s_nop 0
	v_mul_f32_e32 v16, v4, v22
	v_mul_f32_e32 v17, v5, v23
	v_cvt_pk_bf16_f32 v16, v16, v17
	ds_read2_b32 v[18:19], v14 offset0:162 offset1:227
	s_waitcnt lgkmcnt(0)
	v_mul_f32_e32 v17, v6, v18
	v_mul_f32_e32 v18, v7, v19
	v_cvt_pk_bf16_f32 v17, v17, v18
	ds_read2_b32 v[18:19], v15 offset0:36 offset1:101
	s_waitcnt lgkmcnt(0)
	v_mul_f32_e32 v18, v0, v18
	v_mul_f32_e32 v19, v1, v19
	v_cvt_pk_bf16_f32 v18, v18, v19
	ds_read2_b32 v[20:21], v15 offset0:166 offset1:231
	s_waitcnt lgkmcnt(0)
	v_mul_f32_e32 v19, v2, v20
	v_mul_f32_e32 v20, v3, v21
	v_cvt_pk_bf16_f32 v19, v19, v20
	v_add_u32_e32 v20, 32, v24
	v_ashrrev_i32_e32 v21, 31, v20
	v_mul_lo_u32 v22, s56, v21
	v_mul_lo_u32 v23, s57, v20
	v_mad_u64_u32 v[20:21], s[6:7], s56, v20, 0
	v_add3_u32 v21, v21, v22, v23
	ds_read2_b32 v[22:23], v14 offset0:40 offset1:105
	v_lshl_add_u64 v[20:21], v[20:21], 1, s[60:61]
	v_lshl_add_u64 v[20:21], v[20:21], 0, s[4:5]
	v_lshl_add_u64 v[20:21], v[20:21], 0, v[8:9]
	global_store_dwordx4 v[20:21], v[16:19], off sc1
	s_waitcnt lgkmcnt(0)
	s_nop 0
	v_mul_f32_e32 v16, v4, v22
	v_mul_f32_e32 v17, v5, v23
	v_cvt_pk_bf16_f32 v16, v16, v17
	ds_read2_b32 v[18:19], v14 offset0:170 offset1:235
	s_waitcnt lgkmcnt(0)
	v_mul_f32_e32 v17, v6, v18
	v_mul_f32_e32 v18, v7, v19
	v_cvt_pk_bf16_f32 v17, v17, v18
	ds_read2_b32 v[18:19], v15 offset0:44 offset1:109
	s_waitcnt lgkmcnt(0)
	v_mul_f32_e32 v18, v0, v18
	v_mul_f32_e32 v19, v1, v19
	v_cvt_pk_bf16_f32 v18, v18, v19
	ds_read2_b32 v[20:21], v15 offset0:174 offset1:239
	s_waitcnt lgkmcnt(0)
	v_mul_f32_e32 v19, v2, v20
	v_mul_f32_e32 v20, v3, v21
	v_cvt_pk_bf16_f32 v19, v19, v20
	v_add_u32_e32 v20, 40, v24
	v_ashrrev_i32_e32 v21, 31, v20
	v_mul_lo_u32 v22, s56, v21
	v_mul_lo_u32 v23, s57, v20
	v_mad_u64_u32 v[20:21], s[6:7], s56, v20, 0
	v_add3_u32 v21, v21, v22, v23
	ds_read2_b32 v[22:23], v14 offset0:48 offset1:113
	v_lshl_add_u64 v[20:21], v[20:21], 1, s[60:61]
	v_lshl_add_u64 v[20:21], v[20:21], 0, s[4:5]
	v_lshl_add_u64 v[20:21], v[20:21], 0, v[8:9]
	global_store_dwordx4 v[20:21], v[16:19], off sc1
	s_waitcnt lgkmcnt(0)
	s_nop 0
	v_mul_f32_e32 v16, v4, v22
	v_mul_f32_e32 v17, v5, v23
	v_cvt_pk_bf16_f32 v16, v16, v17
	ds_read2_b32 v[18:19], v14 offset0:178 offset1:243
	s_waitcnt lgkmcnt(0)
	v_mul_f32_e32 v17, v6, v18
	v_mul_f32_e32 v18, v7, v19
	v_cvt_pk_bf16_f32 v17, v17, v18
	ds_read2_b32 v[18:19], v15 offset0:52 offset1:117
	s_waitcnt lgkmcnt(0)
	v_mul_f32_e32 v18, v0, v18
	v_mul_f32_e32 v19, v1, v19
	v_cvt_pk_bf16_f32 v18, v18, v19
	ds_read2_b32 v[20:21], v15 offset0:182 offset1:247
	s_waitcnt lgkmcnt(0)
	v_mul_f32_e32 v19, v2, v20
	v_mul_f32_e32 v20, v3, v21
	v_cvt_pk_bf16_f32 v19, v19, v20
	v_add_u32_e32 v20, 48, v24
	v_ashrrev_i32_e32 v21, 31, v20
	v_mul_lo_u32 v22, s56, v21
	v_mul_lo_u32 v23, s57, v20
	v_mad_u64_u32 v[20:21], s[6:7], s56, v20, 0
	v_add3_u32 v21, v21, v22, v23
	ds_read2_b32 v[22:23], v14 offset0:56 offset1:121
	v_lshl_add_u64 v[20:21], v[20:21], 1, s[60:61]
	v_lshl_add_u64 v[20:21], v[20:21], 0, s[4:5]
	v_lshl_add_u64 v[20:21], v[20:21], 0, v[8:9]
	global_store_dwordx4 v[20:21], v[16:19], off sc1
	s_waitcnt lgkmcnt(0)
	v_mul_f32_e32 v4, v4, v22
	v_mul_f32_e32 v5, v5, v23
	v_cvt_pk_bf16_f32 v4, v4, v5
	ds_read2_b32 v[16:17], v14 offset0:186 offset1:251
	s_waitcnt lgkmcnt(0)
	v_mul_f32_e32 v5, v6, v16
	v_mul_f32_e32 v6, v7, v17
	v_cvt_pk_bf16_f32 v5, v5, v6
	ds_read2_b32 v[6:7], v15 offset0:60 offset1:125
	s_waitcnt lgkmcnt(0)
	v_mul_f32_e32 v0, v0, v6
	v_mul_f32_e32 v1, v1, v7
	v_cvt_pk_bf16_f32 v6, v0, v1
	ds_read2_b32 v[0:1], v15 offset0:190 offset1:255
	s_waitcnt lgkmcnt(0)
	v_mul_f32_e32 v0, v2, v0
	v_mul_f32_e32 v1, v3, v1
	v_cvt_pk_bf16_f32 v7, v0, v1
	v_add_u32_e32 v0, 56, v24
	v_ashrrev_i32_e32 v1, 31, v0
	v_mul_lo_u32 v2, s56, v1
	v_mul_lo_u32 v3, s57, v0
	v_mad_u64_u32 v[0:1], s[6:7], s56, v0, 0
	v_add3_u32 v1, v1, v2, v3
	v_lshl_add_u64 v[0:1], v[0:1], 1, s[60:61]
	v_lshl_add_u64 v[0:1], v[0:1], 0, s[4:5]
	v_lshl_add_u64 v[0:1], v[0:1], 0, v[8:9]
	global_store_dwordx4 v[0:1], v[4:7], off sc1
	s_waitcnt lgkmcnt(0)
	s_cbranch_scc0 .Lmy_p0_second

; __device__ __forceinline__ void conv_load(const ConvItem& ci, int lane, float (&v)[64]) {
;     const bool okc = ci.srcc >= 0 && (ci.srcc + lane) < ci.ncols;
;     const float* base = ci.W + (okc ? ci.srcc + lane : 0);
;     const int kmax = ci.Ksrc - 1;
; #pragma unroll
;     for (int i = 0; i < 64; ++i) { const int k = ci.k0 + i, kk = k < kmax ? k : kmax; v[i] = __builtin_nontemporal_load(base + (size_t)kk * ci.ldw); }
; #pragma unroll
;     for (int i = 0; i < 64; ++i) v[i] = (okc && (ci.k0 + i) < ci.Ksrc) ? v[i] : 0.f;
.Lcvp0b_30:
	s_cmp_lt_i32 s58, s76
	s_cselect_b64 s[4:5], -1, 0
	s_and_b64 s[4:5], vcc, s[4:5]
	s_cmp_lt_i32 s64, s76
	s_waitcnt vmcnt(62)
	v_cndmask_b32_e64 v21, 0, v21, s[4:5]
	s_cselect_b64 s[4:5], -1, 0
	s_and_b64 s[4:5], vcc, s[4:5]
	s_cmp_lt_i32 s65, s76
	v_cndmask_b32_e64 v20, 0, v20, s[4:5]
	s_cselect_b64 s[4:5], -1, 0
	s_and_b64 s[4:5], vcc, s[4:5]
	s_cmp_lt_i32 s78, s76
	s_waitcnt vmcnt(61)
	v_cndmask_b32_e64 v19, 0, v19, s[4:5]
	s_cselect_b64 s[4:5], -1, 0
	s_and_b64 s[4:5], vcc, s[4:5]
	s_cmp_lt_i32 s79, s76
	s_waitcnt vmcnt(60)
	v_cndmask_b32_e64 v18, 0, v18, s[4:5]
	s_cselect_b64 s[4:5], -1, 0
	s_and_b64 s[4:5], vcc, s[4:5]
	s_cmp_lt_i32 s80, s76
	s_waitcnt vmcnt(59)
	v_cndmask_b32_e64 v17, 0, v17, s[4:5]
	s_cselect_b64 s[4:5], -1, 0
	s_and_b64 s[4:5], vcc, s[4:5]
	s_cmp_lt_i32 s81, s76
	s_waitcnt vmcnt(58)
	v_cndmask_b32_e64 v16, 0, v16, s[4:5]
	s_cselect_b64 s[4:5], -1, 0
	s_and_b64 s[4:5], vcc, s[4:5]
	s_cmp_lt_i32 s82, s76
	s_waitcnt vmcnt(57)
	v_cndmask_b32_e64 v15, 0, v15, s[4:5]
	s_cselect_b64 s[4:5], -1, 0
	s_and_b64 s[4:5], vcc, s[4:5]
	s_cmp_lt_i32 s83, s76
	s_waitcnt vmcnt(56)
	v_cndmask_b32_e64 v8, 0, v8, s[4:5]
	s_cselect_b64 s[4:5], -1, 0
	s_and_b64 s[4:5], vcc, s[4:5]
	s_cmp_lt_i32 s85, s76
	s_waitcnt vmcnt(55)
	v_cndmask_b32_e64 v29, 0, v29, s[4:5]
	s_cselect_b64 s[4:5], -1, 0
	s_and_b64 s[4:5], vcc, s[4:5]
	s_cmp_lt_i32 s86, s76
	s_waitcnt vmcnt(54)
	v_cndmask_b32_e64 v28, 0, v28, s[4:5]
	s_cselect_b64 s[4:5], -1, 0
	s_and_b64 s[4:5], vcc, s[4:5]
	s_cmp_lt_i32 s87, s76
	s_waitcnt vmcnt(53)
	v_cndmask_b32_e64 v27, 0, v27, s[4:5]
	s_cselect_b64 s[4:5], -1, 0
	s_and_b64 s[4:5], vcc, s[4:5]
	s_cmp_lt_i32 s88, s76
	s_waitcnt vmcnt(52)
	v_cndmask_b32_e64 v26, 0, v26, s[4:5]
	s_cselect_b64 s[4:5], -1, 0
	s_and_b64 s[4:5], vcc, s[4:5]
	s_cmp_lt_i32 s89, s76
	s_waitcnt vmcnt(51)
	v_cndmask_b32_e64 v25, 0, v25, s[4:5]
	s_cselect_b64 s[4:5], -1, 0
	s_and_b64 s[4:5], vcc, s[4:5]
	s_cmp_lt_i32 s90, s76
	s_waitcnt vmcnt(50)
	v_cndmask_b32_e64 v24, 0, v24, s[4:5]
	s_cselect_b64 s[4:5], -1, 0
	s_and_b64 s[4:5], vcc, s[4:5]
	s_cmp_lt_i32 s92, s76
	s_waitcnt vmcnt(49)
	v_cndmask_b32_e64 v23, 0, v23, s[4:5]
	s_cselect_b64 s[4:5], -1, 0
	s_and_b64 s[4:5], vcc, s[4:5]
	s_cmp_lt_i32 s93, s76
	s_waitcnt vmcnt(48)
	v_cndmask_b32_e64 v22, 0, v22, s[4:5]
	s_cselect_b64 s[4:5], -1, 0
	s_and_b64 s[4:5], vcc, s[4:5]
	s_cmp_lt_i32 s94, s76
	s_waitcnt vmcnt(47)
	v_cndmask_b32_e64 v37, 0, v37, s[4:5]
	s_cselect_b64 s[4:5], -1, 0
	s_and_b64 s[4:5], vcc, s[4:5]
	s_cmp_lt_i32 s95, s76
	s_waitcnt vmcnt(46)
	v_cndmask_b32_e64 v36, 0, v36, s[4:5]
	s_cselect_b64 s[4:5], -1, 0
	s_and_b64 s[4:5], vcc, s[4:5]
	s_cmp_lt_i32 s50, s76
	s_waitcnt vmcnt(45)
	v_cndmask_b32_e64 v35, 0, v35, s[4:5]
	s_cselect_b64 s[4:5], -1, 0
	s_and_b64 s[4:5], vcc, s[4:5]
	s_cmp_lt_i32 s51, s76
	s_waitcnt vmcnt(44)
	v_cndmask_b32_e64 v34, 0, v34, s[4:5]
	s_cselect_b64 s[4:5], -1, 0
	s_and_b64 s[4:5], vcc, s[4:5]
	s_cmp_lt_i32 s52, s76
	s_waitcnt vmcnt(43)
	v_cndmask_b32_e64 v33, 0, v33, s[4:5]
	s_cselect_b64 s[4:5], -1, 0
	s_and_b64 s[4:5], vcc, s[4:5]
	s_cmp_lt_i32 s53, s76
	s_waitcnt vmcnt(42)
	v_cndmask_b32_e64 v32, 0, v32, s[4:5]
	s_cselect_b64 s[4:5], -1, 0
	s_and_b64 s[4:5], vcc, s[4:5]
	s_cmp_lt_i32 s6, s76
	s_waitcnt vmcnt(41)
	v_cndmask_b32_e64 v31, 0, v31, s[4:5]
	s_cselect_b64 s[4:5], -1, 0
	s_and_b64 s[4:5], vcc, s[4:5]
	s_cmp_lt_i32 s7, s76
	s_waitcnt vmcnt(40)
	v_cndmask_b32_e64 v30, 0, v30, s[4:5]
	s_cselect_b64 s[4:5], -1, 0
	s_and_b64 s[4:5], vcc, s[4:5]
	s_cmp_lt_i32 s8, s76
	s_waitcnt vmcnt(39)
	v_cndmask_b32_e64 v45, 0, v45, s[4:5]
	s_cselect_b64 s[4:5], -1, 0
	s_and_b64 s[4:5], vcc, s[4:5]
	s_cmp_lt_i32 s9, s76
	s_waitcnt vmcnt(38)
	v_cndmask_b32_e64 v44, 0, v44, s[4:5]
	s_cselect_b64 s[4:5], -1, 0
	s_and_b64 s[4:5], vcc, s[4:5]
	s_cmp_lt_i32 s10, s76
	s_waitcnt vmcnt(37)
	v_cndmask_b32_e64 v43, 0, v43, s[4:5]
	s_cselect_b64 s[4:5], -1, 0
	s_and_b64 s[4:5], vcc, s[4:5]
	s_cmp_lt_i32 s11, s76
	s_waitcnt vmcnt(36)
	v_cndmask_b32_e64 v42, 0, v42, s[4:5]
	s_cselect_b64 s[4:5], -1, 0
	s_and_b64 s[4:5], vcc, s[4:5]
	s_cmp_lt_i32 s14, s76
	s_waitcnt vmcnt(35)
	v_cndmask_b32_e64 v41, 0, v41, s[4:5]
	s_cselect_b64 s[4:5], -1, 0
	s_and_b64 s[4:5], vcc, s[4:5]
	s_cmp_lt_i32 s15, s76
	s_waitcnt vmcnt(34)
	v_cndmask_b32_e64 v40, 0, v40, s[4:5]
	s_cselect_b64 s[4:5], -1, 0
	s_and_b64 s[4:5], vcc, s[4:5]
	s_cmp_lt_i32 s16, s76
	s_waitcnt vmcnt(33)
	v_cndmask_b32_e64 v39, 0, v39, s[4:5]
	s_cselect_b64 s[4:5], -1, 0
	s_and_b64 s[4:5], vcc, s[4:5]
	s_cmp_lt_i32 s17, s76
	s_waitcnt vmcnt(32)
	v_cndmask_b32_e64 v38, 0, v38, s[4:5]
	s_cselect_b64 s[4:5], -1, 0
	s_and_b64 s[4:5], vcc, s[4:5]
	s_cmp_lt_i32 s12, s76
	s_waitcnt vmcnt(31)
	v_cndmask_b32_e64 v53, 0, v53, s[4:5]
	s_cselect_b64 s[4:5], -1, 0
	s_and_b64 s[4:5], vcc, s[4:5]
	s_cmp_lt_i32 s13, s76
	s_waitcnt vmcnt(30)
	v_cndmask_b32_e64 v52, 0, v52, s[4:5]
	s_cselect_b64 s[4:5], -1, 0
	s_and_b64 s[4:5], vcc, s[4:5]
	s_cmp_lt_i32 s20, s76
	s_waitcnt vmcnt(29)
	v_cndmask_b32_e64 v51, 0, v51, s[4:5]
	s_cselect_b64 s[4:5], -1, 0
	s_and_b64 s[4:5], vcc, s[4:5]
	s_cmp_lt_i32 s21, s76
	s_waitcnt vmcnt(28)
	v_cndmask_b32_e64 v50, 0, v50, s[4:5]
	s_cselect_b64 s[4:5], -1, 0
	s_and_b64 s[4:5], vcc, s[4:5]
	s_cmp_lt_i32 s24, s76
	s_waitcnt vmcnt(27)
	v_cndmask_b32_e64 v49, 0, v49, s[4:5]
	s_cselect_b64 s[4:5], -1, 0
	s_and_b64 s[4:5], vcc, s[4:5]
	s_cmp_lt_i32 s25, s76
	s_waitcnt vmcnt(26)
	v_cndmask_b32_e64 v48, 0, v48, s[4:5]
	s_cselect_b64 s[4:5], -1, 0
	s_and_b64 s[4:5], vcc, s[4:5]
	s_cmp_lt_i32 s26, s76
	s_waitcnt vmcnt(25)
	v_cndmask_b32_e64 v47, 0, v47, s[4:5]
	s_cselect_b64 s[4:5], -1, 0
	s_and_b64 s[4:5], vcc, s[4:5]
	s_cmp_lt_i32 s27, s76
	s_waitcnt vmcnt(24)
; #define LAS __attribute__((address_space(3)))
; #define LDS_WAIT() asm volatile("s_waitcnt lgkmcnt(0)" ::: "memory")
; __device__ __forceinline__ void conv_load(const ConvItem& ci, int lane, float (&v)[64]) {
;     ...
;     for (int i = 0; i < 64; ++i) v[i] = (okc && (ci.k0 + i) < ci.Ksrc) ? v[i] : 0.f;
; }
; __device__ __forceinline__ void conv_store(const ConvItem& ci, LAS float* scr, int lane, const float (&v)[64]) {
;     const int c = lane & 7;
;     f32x4 s0 = {1.f, 1.f, 1.f, 1.f}, s1 = s0;
;     if (ci.ks) { const int kb = ci.k0 + 8 * c < ci.Ksrc - 8 ? ci.k0 + 8 * c : ci.Ksrc - 8; s0 = *(const f32x4*)(ci.ks + kb); s1 = *(const f32x4*)(ci.ks + kb + 4); }
; #pragma unroll
;     for (int i = 0; i < 64; ++i) scr[i * 65 + lane] = v[i];
;     LDS_WAIT(); asm volatile("" ::: "memory");
	v_cndmask_b32_e64 v46, 0, v46, s[4:5]
	s_cselect_b64 s[4:5], -1, 0
	s_and_b64 s[4:5], vcc, s[4:5]
	s_cmp_lt_i32 s18, s76
	s_waitcnt vmcnt(23)
	v_cndmask_b32_e64 v61, 0, v61, s[4:5]
	s_cselect_b64 s[4:5], -1, 0
	s_and_b64 s[4:5], vcc, s[4:5]
	s_cmp_lt_i32 s19, s76
	s_waitcnt vmcnt(22)
	v_cndmask_b32_e64 v60, 0, v60, s[4:5]
	s_cselect_b64 s[4:5], -1, 0
	s_and_b64 s[4:5], vcc, s[4:5]
	s_cmp_lt_i32 s28, s76
	s_waitcnt vmcnt(21)
	v_cndmask_b32_e64 v59, 0, v59, s[4:5]
	s_cselect_b64 s[4:5], -1, 0
	s_and_b64 s[4:5], vcc, s[4:5]
	s_cmp_lt_i32 s29, s76
	s_waitcnt vmcnt(20)
	v_cndmask_b32_e64 v58, 0, v58, s[4:5]
	s_cselect_b64 s[4:5], -1, 0
	s_and_b64 s[4:5], vcc, s[4:5]
	s_cmp_lt_i32 s22, s76
	s_waitcnt vmcnt(19)
	v_cndmask_b32_e64 v57, 0, v57, s[4:5]
	s_cselect_b64 s[4:5], -1, 0
	s_and_b64 s[4:5], vcc, s[4:5]
	s_cmp_lt_i32 s23, s76
	s_waitcnt vmcnt(18)
	v_cndmask_b32_e64 v56, 0, v56, s[4:5]
	s_cselect_b64 s[4:5], -1, 0
	s_and_b64 s[4:5], vcc, s[4:5]
	s_cmp_lt_i32 s30, s76
	s_waitcnt vmcnt(17)
	v_cndmask_b32_e64 v55, 0, v55, s[4:5]
	s_cselect_b64 s[4:5], -1, 0
	s_and_b64 s[4:5], vcc, s[4:5]
	s_cmp_lt_i32 s31, s76
	s_waitcnt vmcnt(16)
	v_cndmask_b32_e64 v54, 0, v54, s[4:5]
	s_cselect_b64 s[4:5], -1, 0
	s_and_b64 s[4:5], vcc, s[4:5]
	s_cmp_lt_i32 s36, s76
	s_waitcnt vmcnt(15)
	v_cndmask_b32_e64 v70, 0, v70, s[4:5]
	s_cselect_b64 s[4:5], -1, 0
	s_and_b64 s[4:5], vcc, s[4:5]
	s_cmp_lt_i32 s37, s76
	s_waitcnt vmcnt(14)
	v_cndmask_b32_e64 v69, 0, v69, s[4:5]
	s_cselect_b64 s[4:5], -1, 0
	s_and_b64 s[4:5], vcc, s[4:5]
	s_cmp_lt_i32 s38, s76
	s_waitcnt vmcnt(13)
	v_cndmask_b32_e64 v68, 0, v68, s[4:5]
	s_cselect_b64 s[4:5], -1, 0
	s_and_b64 s[4:5], vcc, s[4:5]
	s_cmp_lt_i32 s39, s76
	s_waitcnt vmcnt(12)
	v_cndmask_b32_e64 v67, 0, v67, s[4:5]
	s_cselect_b64 s[4:5], -1, 0
	s_and_b64 s[4:5], vcc, s[4:5]
	s_cmp_lt_i32 s34, s76
	s_waitcnt vmcnt(11)
	v_cndmask_b32_e64 v66, 0, v66, s[4:5]
	s_cselect_b64 s[4:5], -1, 0
	s_and_b64 s[4:5], vcc, s[4:5]
	s_cmp_lt_i32 s35, s76
	s_waitcnt vmcnt(10)
	v_cndmask_b32_e64 v64, 0, v64, s[4:5]
	s_cselect_b64 s[4:5], -1, 0
	s_and_b64 s[4:5], vcc, s[4:5]
	s_cmp_lt_i32 s42, s76
	s_waitcnt vmcnt(9)
	v_cndmask_b32_e64 v63, 0, v63, s[4:5]
	s_cselect_b64 s[4:5], -1, 0
	s_and_b64 s[4:5], vcc, s[4:5]
	s_cmp_lt_i32 s43, s76
	s_waitcnt vmcnt(8)
	v_cndmask_b32_e64 v62, 0, v62, s[4:5]
	s_cselect_b64 s[4:5], -1, 0
	s_and_b64 s[4:5], vcc, s[4:5]
	s_cmp_lt_i32 s54, s76
	s_waitcnt vmcnt(7)
	v_cndmask_b32_e64 v65, 0, v65, s[4:5]
	s_cselect_b64 s[4:5], -1, 0
	s_and_b64 s[4:5], vcc, s[4:5]
	s_cmp_lt_i32 s55, s76
	s_waitcnt vmcnt(6)
	v_cndmask_b32_e64 v74, 0, v74, s[4:5]
	s_cselect_b64 s[4:5], -1, 0
	s_and_b64 s[4:5], vcc, s[4:5]
	s_cmp_lt_i32 s46, s76
	ds_write2_b32 v12, v21, v20 offset1:65
	ds_write2_b32 v12, v19, v18 offset0:130 offset1:195
	v_add_u32_e32 v18, 0x400, v12
	s_waitcnt vmcnt(5)
	v_cndmask_b32_e64 v73, 0, v73, s[4:5]
	s_cselect_b64 s[4:5], -1, 0
	ds_write2_b32 v18, v17, v16 offset0:4 offset1:69
	ds_write2_b32 v18, v15, v8 offset0:134 offset1:199
	v_add_u32_e32 v8, 0x800, v12
	s_and_b64 s[4:5], vcc, s[4:5]
	ds_write2_b32 v8, v29, v28 offset0:8 offset1:73
	ds_write2_b32 v8, v27, v26 offset0:138 offset1:203
	v_add_u32_e32 v8, 0xc00, v12
	s_cmp_lt_i32 s47, s76
	ds_write2_b32 v8, v25, v24 offset0:12 offset1:77
	ds_write2_b32 v8, v23, v22 offset0:142 offset1:207
	v_add_u32_e32 v8, 0x1000, v12
	s_waitcnt vmcnt(4)
	v_cndmask_b32_e64 v72, 0, v72, s[4:5]
	s_cselect_b64 s[4:5], -1, 0
	ds_write2_b32 v8, v37, v36 offset0:16 offset1:81
	ds_write2_b32 v8, v35, v34 offset0:146 offset1:211
	v_add_u32_e32 v8, 0x1400, v12
	s_and_b64 s[4:5], vcc, s[4:5]
	ds_write2_b32 v8, v33, v32 offset0:20 offset1:85
	ds_write2_b32 v8, v31, v30 offset0:150 offset1:215
	v_add_u32_e32 v8, 0x1800, v12
	s_cmp_lt_i32 s48, s76
	ds_write2_b32 v8, v45, v44 offset0:24 offset1:89
	ds_write2_b32 v8, v43, v42 offset0:154 offset1:219
	v_add_u32_e32 v8, 0x1c00, v12
	s_waitcnt vmcnt(3)
	v_cndmask_b32_e64 v71, 0, v71, s[4:5]
	s_cselect_b64 s[4:5], -1, 0
	ds_write2_b32 v8, v41, v40 offset0:28 offset1:93
	ds_write2_b32 v8, v39, v38 offset0:158 offset1:223
	v_add_u32_e32 v8, 0x2000, v12
	s_and_b64 s[4:5], vcc, s[4:5]
	ds_write2_b32 v8, v53, v52 offset0:32 offset1:97
	ds_write2_b32 v8, v51, v50 offset0:162 offset1:227
	v_add_u32_e32 v8, 0x2400, v12
	s_cmp_lt_i32 s49, s76
	ds_write2_b32 v8, v49, v48 offset0:36 offset1:101
	ds_write2_b32 v8, v47, v46 offset0:166 offset1:231
	v_add_u32_e32 v8, 0x2800, v12
	s_waitcnt vmcnt(2)
	v_cndmask_b32_e64 v77, 0, v77, s[4:5]
	s_cselect_b64 s[4:5], -1, 0
	ds_write2_b32 v8, v61, v60 offset0:40 offset1:105
	ds_write2_b32 v8, v59, v58 offset0:170 offset1:235
	v_add_u32_e32 v8, 0x2c00, v12
	s_and_b64 s[4:5], vcc, s[4:5]
	ds_write2_b32 v8, v57, v56 offset0:44 offset1:109
	ds_write2_b32 v8, v55, v54 offset0:174 offset1:239
	v_add_u32_e32 v8, 0x3000, v12
	s_cmp_lt_i32 s44, s76
	ds_write2_b32 v8, v70, v69 offset0:48 offset1:113
	ds_write2_b32 v8, v68, v67 offset0:178 offset1:243
	v_add_u32_e32 v8, 0x3400, v12
	s_waitcnt vmcnt(1)
	v_cndmask_b32_e64 v76, 0, v76, s[4:5]
	s_cselect_b64 s[4:5], -1, 0
	ds_write2_b32 v8, v66, v64 offset0:52 offset1:117
	ds_write2_b32 v8, v63, v62 offset0:182 offset1:247
	v_add_u32_e32 v8, 0x3800, v12
	s_and_b64 vcc, vcc, s[4:5]
	ds_write2_b32 v8, v65, v74 offset0:56 offset1:121
	ds_write2_b32 v8, v73, v72 offset0:186 offset1:251
	v_add_u32_e32 v8, 0x3c00, v12
	s_waitcnt vmcnt(0)
	v_cndmask_b32_e32 v75, 0, v75, vcc
	ds_write2_b32 v8, v71, v77 offset0:60 offset1:125
	ds_write2_b32 v8, v76, v75 offset0:190 offset1:255
	s_waitcnt lgkmcnt(0)
; __device__ __forceinline__ unsigned cvt_pk_bf16(float lo, float hi) { unsigned r; asm volatile("v_cvt_pk_bf16_f32 %0, %1, %2" : "=v"(r) : "v"(lo), "v"(hi)); return r; }
; #define LAS __attribute__((address_space(3)))
; #define LDS_WAIT() asm volatile("s_waitcnt lgkmcnt(0)" ::: "memory")
; __device__ __forceinline__ void conv_store(const ConvItem& ci, LAS float* scr, int lane, const float (&v)[64]) {
;     ...
;     LDS_WAIT(); asm volatile("" ::: "memory");
; #pragma unroll
;     for (int j = 0; j < 8; ++j) { const int n = (lane >> 3) + 8 * j; const LAS float* s = scr + (8 * c) * 65 + n;
;         v4u o; o.x = cvt_pk_bf16(s[0 * 65] * s0[0], s[1 * 65] * s0[1]); o.y = cvt_pk_bf16(s[2 * 65] * s0[2], s[3 * 65] * s0[3]); o.z = cvt_pk_bf16(s[4 * 65] * s1[0], s[5 * 65] * s1[1]); o.w = cvt_pk_bf16(s[6 * 65] * s1[2], s[7 * 65] * s1[3]);
;         *(v4u*)(ci.dst + (size_t)(ci.drow0 + n) * ci.ldd + ci.k0 + 8 * c) = o; }
	v_add_u32_e32 v192, 0x400, v14
	ds_read2_b32 v[128:129], v14 offset1:65
	ds_read2_b32 v[130:131], v14 offset0:130 offset1:195
	ds_read2_b32 v[132:133], v192 offset0:4 offset1:69
	ds_read2_b32 v[134:135], v192 offset0:134 offset1:199
	ds_read2_b32 v[136:137], v14 offset0:8 offset1:73
	ds_read2_b32 v[138:139], v14 offset0:138 offset1:203
	ds_read2_b32 v[140:141], v192 offset0:12 offset1:77
	ds_read2_b32 v[142:143], v192 offset0:142 offset1:207
	ds_read2_b32 v[144:145], v14 offset0:16 offset1:81
	ds_read2_b32 v[146:147], v14 offset0:146 offset1:211
	ds_read2_b32 v[148:149], v192 offset0:20 offset1:85
	ds_read2_b32 v[150:151], v192 offset0:150 offset1:215
	ds_read2_b32 v[152:153], v14 offset0:24 offset1:89
	ds_read2_b32 v[154:155], v14 offset0:154 offset1:219
	ds_read2_b32 v[156:157], v192 offset0:28 offset1:93
	ds_read2_b32 v[158:159], v192 offset0:158 offset1:223
	ds_read2_b32 v[160:161], v14 offset0:32 offset1:97
	ds_read2_b32 v[162:163], v14 offset0:162 offset1:227
	ds_read2_b32 v[164:165], v192 offset0:36 offset1:101
	ds_read2_b32 v[166:167], v192 offset0:166 offset1:231
	ds_read2_b32 v[168:169], v14 offset0:40 offset1:105
	ds_read2_b32 v[170:171], v14 offset0:170 offset1:235
	ds_read2_b32 v[172:173], v192 offset0:44 offset1:109
	ds_read2_b32 v[174:175], v192 offset0:174 offset1:239
	ds_read2_b32 v[176:177], v14 offset0:48 offset1:113
	ds_read2_b32 v[178:179], v14 offset0:178 offset1:243
	ds_read2_b32 v[180:181], v192 offset0:52 offset1:117
	ds_read2_b32 v[182:183], v192 offset0:182 offset1:247
	ds_read2_b32 v[184:185], v14 offset0:56 offset1:121
	ds_read2_b32 v[186:187], v14 offset0:186 offset1:251
	ds_read2_b32 v[188:189], v192 offset0:60 offset1:125
	ds_read2_b32 v[190:191], v192 offset0:190 offset1:255
	s_waitcnt lgkmcnt(0)
	v_add_u32_e32 v24, s59, v13
	v_mul_lo_u32 v22, s57, v24
	s_ashr_i32 s59, s58, 31
	v_readlane_b32 s76, v254, 31
	s_waitcnt lgkmcnt(0)
	v_mul_f32_e32 v8, v4, v128
	v_mul_f32_e32 v15, v5, v129
	v_cvt_pk_bf16_f32 v16, v8, v15
	s_add_i32 s3, s3, s33
	s_add_i32 s66, s66, s67
	s_add_i32 s68, s68, s69
	s_add_i32 s70, s70, s71
	s_waitcnt lgkmcnt(0)
	v_mul_f32_e32 v15, v7, v131
	v_mul_f32_e32 v8, v6, v130
	v_cvt_pk_bf16_f32 v17, v8, v15
	v_add_u32_e32 v15, 0x400, v14
	s_add_i32 s72, s72, s73
	s_add_i32 s74, s74, s75
	v_readlane_b32 s78, v254, 33
	v_readlane_b32 s79, v254, 34
	s_waitcnt lgkmcnt(0)
	v_mul_f32_e32 v8, v0, v132
	v_mul_f32_e32 v18, v1, v133
	v_cvt_pk_bf16_f32 v18, v8, v18
	v_readlane_b32 s80, v255, 21
	v_readlane_b32 s77, v254, 32
	s_movk_i32 s78, 0x1580
	v_readlane_b32 s82, v255, 23
	s_waitcnt lgkmcnt(0)
	v_mul_f32_e32 v8, v2, v134
	v_mul_f32_e32 v19, v3, v135
	v_cvt_pk_bf16_f32 v19, v8, v19
	v_ashrrev_i32_e32 v8, 31, v24
	v_mul_lo_u32 v8, s56, v8
	v_mad_u64_u32 v[20:21], s[4:5], s56, v24, 0
	v_add3_u32 v21, v21, v8, v22
	v_lshl_add_u64 v[20:21], v[20:21], 1, s[60:61]
	s_lshl_b64 s[4:5], s[58:59], 1
	v_lshl_add_u64 v[20:21], v[20:21], 0, s[4:5]
	v_lshlrev_b32_e32 v8, 1, v10
	v_lshl_add_u64 v[20:21], v[20:21], 0, v[8:9]
	global_store_dwordx4 v[20:21], v[16:19], off sc1
	s_cmpk_lt_i32 s3, 27072
	v_readlane_b32 s83, v255, 24
	s_waitcnt lgkmcnt(0)
	v_mul_f32_e32 v16, v4, v136
	v_mul_f32_e32 v17, v5, v137
	v_cvt_pk_bf16_f32 v16, v16, v17
	s_mov_b32 s79, 0x3f22f983
	s_mov_b32 s85, 0xbfc90fda
	s_brev_b32 s86, 1
	s_movk_i32 s87, 0x1f8
	s_waitcnt lgkmcnt(0)
	v_mul_f32_e32 v17, v6, v138
	v_mul_f32_e32 v18, v7, v139
	v_cvt_pk_bf16_f32 v17, v17, v18
	s_mov_b64 s[88:89], 0x80
	s_mov_b64 s[92:93], 0x4000
	s_mov_b64 s[94:95], 0x4800
	v_readlane_b32 s81, v255, 22
	s_waitcnt lgkmcnt(0)
	v_mul_f32_e32 v18, v0, v140
	v_mul_f32_e32 v19, v1, v141
	v_cvt_pk_bf16_f32 v18, v18, v19
	s_waitcnt lgkmcnt(0)
	v_mul_f32_e32 v19, v2, v142
	v_mul_f32_e32 v20, v3, v143
	v_cvt_pk_bf16_f32 v19, v19, v20
	v_add_u32_e32 v20, 8, v24
	v_ashrrev_i32_e32 v21, 31, v20
	v_mul_lo_u32 v22, s56, v21
	v_mul_lo_u32 v23, s57, v20
	v_mad_u64_u32 v[20:21], s[6:7], s56, v20, 0
	v_add3_u32 v21, v21, v22, v23
	v_lshl_add_u64 v[20:21], v[20:21], 1, s[60:61]
	v_lshl_add_u64 v[20:21], v[20:21], 0, s[4:5]
	v_lshl_add_u64 v[20:21], v[20:21], 0, v[8:9]
	global_store_dwordx4 v[20:21], v[16:19], off sc1
	s_waitcnt lgkmcnt(0)
	s_nop 0
	v_mul_f32_e32 v16, v4, v144
	v_mul_f32_e32 v17, v5, v145
	v_cvt_pk_bf16_f32 v16, v16, v17
	s_waitcnt lgkmcnt(0)
	v_mul_f32_e32 v17, v6, v146
	v_mul_f32_e32 v18, v7, v147
	v_cvt_pk_bf16_f32 v17, v17, v18
	s_waitcnt lgkmcnt(0)
	v_mul_f32_e32 v18, v0, v148
	v_mul_f32_e32 v19, v1, v149
	v_cvt_pk_bf16_f32 v18, v18, v19
	s_waitcnt lgkmcnt(0)
; __device__ __forceinline__ unsigned cvt_pk_bf16(float lo, float hi) { unsigned r; asm volatile("v_cvt_pk_bf16_f32 %0, %1, %2" : "=v"(r) : "v"(lo), "v"(hi)); return r; }
; #define LAS __attribute__((address_space(3)))
; __device__ __forceinline__ void conv_store(const ConvItem& ci, LAS float* scr, int lane, const float (&v)[64]) {
;     ...
;     for (int j = 0; j < 8; ++j) { const int n = (lane >> 3) + 8 * j; const LAS float* s = scr + (8 * c) * 65 + n;
;         v4u o; o.x = cvt_pk_bf16(s[0 * 65] * s0[0], s[1 * 65] * s0[1]); o.y = cvt_pk_bf16(s[2 * 65] * s0[2], s[3 * 65] * s0[3]); o.z = cvt_pk_bf16(s[4 * 65] * s1[0], s[5 * 65] * s1[1]); o.w = cvt_pk_bf16(s[6 * 65] * s1[2], s[7 * 65] * s1[3]);
;         *(v4u*)(ci.dst + (size_t)(ci.drow0 + n) * ci.ldd + ci.k0 + 8 * c) = o; }
	v_mul_f32_e32 v19, v2, v150
	v_mul_f32_e32 v20, v3, v151
	v_cvt_pk_bf16_f32 v19, v19, v20
	v_add_u32_e32 v20, 16, v24
	v_ashrrev_i32_e32 v21, 31, v20
	v_mul_lo_u32 v22, s56, v21
	v_mul_lo_u32 v23, s57, v20
	v_mad_u64_u32 v[20:21], s[6:7], s56, v20, 0
	v_add3_u32 v21, v21, v22, v23
	v_lshl_add_u64 v[20:21], v[20:21], 1, s[60:61]
	v_lshl_add_u64 v[20:21], v[20:21], 0, s[4:5]
	v_lshl_add_u64 v[20:21], v[20:21], 0, v[8:9]
	global_store_dwordx4 v[20:21], v[16:19], off sc1
	s_waitcnt lgkmcnt(0)
	s_nop 0
	v_mul_f32_e32 v16, v4, v152
	v_mul_f32_e32 v17, v5, v153
	v_cvt_pk_bf16_f32 v16, v16, v17
	s_waitcnt lgkmcnt(0)
	v_mul_f32_e32 v17, v6, v154
	v_mul_f32_e32 v18, v7, v155
	v_cvt_pk_bf16_f32 v17, v17, v18
	s_waitcnt lgkmcnt(0)
	v_mul_f32_e32 v18, v0, v156
	v_mul_f32_e32 v19, v1, v157
	v_cvt_pk_bf16_f32 v18, v18, v19
	s_waitcnt lgkmcnt(0)
	v_mul_f32_e32 v19, v2, v158
	v_mul_f32_e32 v20, v3, v159
	v_cvt_pk_bf16_f32 v19, v19, v20
	v_add_u32_e32 v20, 24, v24
	v_ashrrev_i32_e32 v21, 31, v20
	v_mul_lo_u32 v22, s56, v21
	v_mul_lo_u32 v23, s57, v20
	v_mad_u64_u32 v[20:21], s[6:7], s56, v20, 0
	v_add3_u32 v21, v21, v22, v23
	v_lshl_add_u64 v[20:21], v[20:21], 1, s[60:61]
	v_lshl_add_u64 v[20:21], v[20:21], 0, s[4:5]
	v_lshl_add_u64 v[20:21], v[20:21], 0, v[8:9]
	global_store_dwordx4 v[20:21], v[16:19], off sc1
	s_waitcnt lgkmcnt(0)
	s_nop 0
	v_mul_f32_e32 v16, v4, v160
	v_mul_f32_e32 v17, v5, v161
	v_cvt_pk_bf16_f32 v16, v16, v17
	s_waitcnt lgkmcnt(0)
	v_mul_f32_e32 v17, v6, v162
	v_mul_f32_e32 v18, v7, v163
	v_cvt_pk_bf16_f32 v17, v17, v18
	s_waitcnt lgkmcnt(0)
	v_mul_f32_e32 v18, v0, v164
	v_mul_f32_e32 v19, v1, v165
	v_cvt_pk_bf16_f32 v18, v18, v19
	s_waitcnt lgkmcnt(0)
	v_mul_f32_e32 v19, v2, v166
	v_mul_f32_e32 v20, v3, v167
	v_cvt_pk_bf16_f32 v19, v19, v20
	v_add_u32_e32 v20, 32, v24
	v_ashrrev_i32_e32 v21, 31, v20
	v_mul_lo_u32 v22, s56, v21
	v_mul_lo_u32 v23, s57, v20
	v_mad_u64_u32 v[20:21], s[6:7], s56, v20, 0
	v_add3_u32 v21, v21, v22, v23
	v_lshl_add_u64 v[20:21], v[20:21], 1, s[60:61]
	v_lshl_add_u64 v[20:21], v[20:21], 0, s[4:5]
	v_lshl_add_u64 v[20:21], v[20:21], 0, v[8:9]
	global_store_dwordx4 v[20:21], v[16:19], off sc1
	s_waitcnt lgkmcnt(0)
	s_nop 0
	v_mul_f32_e32 v16, v4, v168
	v_mul_f32_e32 v17, v5, v169
	v_cvt_pk_bf16_f32 v16, v16, v17
	s_waitcnt lgkmcnt(0)
	v_mul_f32_e32 v17, v6, v170
	v_mul_f32_e32 v18, v7, v171
	v_cvt_pk_bf16_f32 v17, v17, v18
	s_waitcnt lgkmcnt(0)
	v_mul_f32_e32 v18, v0, v172
	v_mul_f32_e32 v19, v1, v173
	v_cvt_pk_bf16_f32 v18, v18, v19
	s_waitcnt lgkmcnt(0)
	v_mul_f32_e32 v19, v2, v174
	v_mul_f32_e32 v20, v3, v175
	v_cvt_pk_bf16_f32 v19, v19, v20
	v_add_u32_e32 v20, 40, v24
	v_ashrrev_i32_e32 v21, 31, v20
	v_mul_lo_u32 v22, s56, v21
	v_mul_lo_u32 v23, s57, v20
	v_mad_u64_u32 v[20:21], s[6:7], s56, v20, 0
	v_add3_u32 v21, v21, v22, v23
	v_lshl_add_u64 v[20:21], v[20:21], 1, s[60:61]
	v_lshl_add_u64 v[20:21], v[20:21], 0, s[4:5]
	v_lshl_add_u64 v[20:21], v[20:21], 0, v[8:9]
	global_store_dwordx4 v[20:21], v[16:19], off sc1
	s_waitcnt lgkmcnt(0)
	s_nop 0
	v_mul_f32_e32 v16, v4, v176
	v_mul_f32_e32 v17, v5, v177
	v_cvt_pk_bf16_f32 v16, v16, v17
	s_waitcnt lgkmcnt(0)
	v_mul_f32_e32 v17, v6, v178
	v_mul_f32_e32 v18, v7, v179
	v_cvt_pk_bf16_f32 v17, v17, v18
	s_waitcnt lgkmcnt(0)
	v_mul_f32_e32 v18, v0, v180
	v_mul_f32_e32 v19, v1, v181
	v_cvt_pk_bf16_f32 v18, v18, v19
	s_waitcnt lgkmcnt(0)
	v_mul_f32_e32 v19, v2, v182
	v_mul_f32_e32 v20, v3, v183
	v_cvt_pk_bf16_f32 v19, v19, v20
	v_add_u32_e32 v20, 48, v24
	v_ashrrev_i32_e32 v21, 31, v20
	v_mul_lo_u32 v22, s56, v21
	v_mul_lo_u32 v23, s57, v20
	v_mad_u64_u32 v[20:21], s[6:7], s56, v20, 0
	v_add3_u32 v21, v21, v22, v23
	v_lshl_add_u64 v[20:21], v[20:21], 1, s[60:61]
	v_lshl_add_u64 v[20:21], v[20:21], 0, s[4:5]
	v_lshl_add_u64 v[20:21], v[20:21], 0, v[8:9]
	global_store_dwordx4 v[20:21], v[16:19], off sc1
	s_waitcnt lgkmcnt(0)
	v_mul_f32_e32 v4, v4, v184
	v_mul_f32_e32 v5, v5, v185
	v_cvt_pk_bf16_f32 v4, v4, v5
	s_waitcnt lgkmcnt(0)
	v_mul_f32_e32 v5, v6, v186
	v_mul_f32_e32 v6, v7, v187
	v_cvt_pk_bf16_f32 v5, v5, v6
	s_waitcnt lgkmcnt(0)
	v_mul_f32_e32 v0, v0, v188
	v_mul_f32_e32 v1, v1, v189
	v_cvt_pk_bf16_f32 v6, v0, v1
	s_waitcnt lgkmcnt(0)
	v_mul_f32_e32 v0, v2, v190
	v_mul_f32_e32 v1, v3, v191
	v_cvt_pk_bf16_f32 v7, v0, v1
	v_add_u32_e32 v0, 56, v24
	v_ashrrev_i32_e32 v1, 31, v0
	v_mul_lo_u32 v2, s56, v1
	v_mul_lo_u32 v3, s57, v0
	v_mad_u64_u32 v[0:1], s[6:7], s56, v0, 0
	v_add3_u32 v1, v1, v2, v3
	v_lshl_add_u64 v[0:1], v[0:1], 1, s[60:61]
	v_lshl_add_u64 v[0:1], v[0:1], 0, s[4:5]
	v_lshl_add_u64 v[0:1], v[0:1], 0, v[8:9]
	global_store_dwordx4 v[0:1], v[4:7], off sc1
	s_waitcnt lgkmcnt(0)
	s_cbranch_scc0 .Lcvp0b_ret

; __device__ __forceinline__ void conv_load(const ConvItem& ci, int lane, float (&v)[64]) {
;     const bool okc = ci.srcc >= 0 && (ci.srcc + lane) < ci.ncols;
;     const float* base = ci.W + (okc ? ci.srcc + lane : 0);
;     const int kmax = ci.Ksrc - 1;
; #pragma unroll
;     for (int i = 0; i < 64; ++i) { const int k = ci.k0 + i, kk = k < kmax ? k : kmax; v[i] = __builtin_nontemporal_load(base + (size_t)kk * ci.ldw); }
; #pragma unroll
;     for (int i = 0; i < 64; ++i) v[i] = (okc && (ci.k0 + i) < ci.Ksrc) ? v[i] : 0.f;
.Lcvp0c_30:
	s_cmp_lt_i32 s58, s76
	s_cselect_b64 s[4:5], -1, 0
	s_and_b64 s[4:5], vcc, s[4:5]
	s_cmp_lt_i32 s64, s76
	s_waitcnt vmcnt(62)
	v_cndmask_b32_e64 v21, 0, v21, s[4:5]
	s_cselect_b64 s[4:5], -1, 0
	s_and_b64 s[4:5], vcc, s[4:5]
	s_cmp_lt_i32 s65, s76
	v_cndmask_b32_e64 v20, 0, v20, s[4:5]
	s_cselect_b64 s[4:5], -1, 0
	s_and_b64 s[4:5], vcc, s[4:5]
	s_cmp_lt_i32 s78, s76
	s_waitcnt vmcnt(61)
	v_cndmask_b32_e64 v19, 0, v19, s[4:5]
	s_cselect_b64 s[4:5], -1, 0
	s_and_b64 s[4:5], vcc, s[4:5]
	s_cmp_lt_i32 s79, s76
	s_waitcnt vmcnt(60)
	v_cndmask_b32_e64 v18, 0, v18, s[4:5]
	s_cselect_b64 s[4:5], -1, 0
	s_and_b64 s[4:5], vcc, s[4:5]
	s_cmp_lt_i32 s80, s76
	s_waitcnt vmcnt(59)
	v_cndmask_b32_e64 v17, 0, v17, s[4:5]
	s_cselect_b64 s[4:5], -1, 0
	s_and_b64 s[4:5], vcc, s[4:5]
	s_cmp_lt_i32 s81, s76
	s_waitcnt vmcnt(58)
	v_cndmask_b32_e64 v16, 0, v16, s[4:5]
	s_cselect_b64 s[4:5], -1, 0
	s_and_b64 s[4:5], vcc, s[4:5]
	s_cmp_lt_i32 s82, s76
	s_waitcnt vmcnt(57)
	v_cndmask_b32_e64 v15, 0, v15, s[4:5]
	s_cselect_b64 s[4:5], -1, 0
	s_and_b64 s[4:5], vcc, s[4:5]
	s_cmp_lt_i32 s83, s76
	s_waitcnt vmcnt(56)
	v_cndmask_b32_e64 v8, 0, v8, s[4:5]
	s_cselect_b64 s[4:5], -1, 0
	s_and_b64 s[4:5], vcc, s[4:5]
	s_cmp_lt_i32 s85, s76
	s_waitcnt vmcnt(55)
	v_cndmask_b32_e64 v29, 0, v29, s[4:5]
	s_cselect_b64 s[4:5], -1, 0
	s_and_b64 s[4:5], vcc, s[4:5]
	s_cmp_lt_i32 s86, s76
	s_waitcnt vmcnt(54)
	v_cndmask_b32_e64 v28, 0, v28, s[4:5]
	s_cselect_b64 s[4:5], -1, 0
	s_and_b64 s[4:5], vcc, s[4:5]
	s_cmp_lt_i32 s87, s76
	s_waitcnt vmcnt(53)
	v_cndmask_b32_e64 v27, 0, v27, s[4:5]
	s_cselect_b64 s[4:5], -1, 0
	s_and_b64 s[4:5], vcc, s[4:5]
	s_cmp_lt_i32 s88, s76
	s_waitcnt vmcnt(52)
	v_cndmask_b32_e64 v26, 0, v26, s[4:5]
	s_cselect_b64 s[4:5], -1, 0
	s_and_b64 s[4:5], vcc, s[4:5]
	s_cmp_lt_i32 s89, s76
	s_waitcnt vmcnt(51)
	v_cndmask_b32_e64 v25, 0, v25, s[4:5]
	s_cselect_b64 s[4:5], -1, 0
	s_and_b64 s[4:5], vcc, s[4:5]
	s_cmp_lt_i32 s90, s76
	s_waitcnt vmcnt(50)
	v_cndmask_b32_e64 v24, 0, v24, s[4:5]
	s_cselect_b64 s[4:5], -1, 0
	s_and_b64 s[4:5], vcc, s[4:5]
	s_cmp_lt_i32 s92, s76
	s_waitcnt vmcnt(49)
	v_cndmask_b32_e64 v23, 0, v23, s[4:5]
	s_cselect_b64 s[4:5], -1, 0
	s_and_b64 s[4:5], vcc, s[4:5]
	s_cmp_lt_i32 s93, s76
	s_waitcnt vmcnt(48)
	v_cndmask_b32_e64 v22, 0, v22, s[4:5]
	s_cselect_b64 s[4:5], -1, 0
	s_and_b64 s[4:5], vcc, s[4:5]
	s_cmp_lt_i32 s94, s76
	s_waitcnt vmcnt(47)
	v_cndmask_b32_e64 v37, 0, v37, s[4:5]
	s_cselect_b64 s[4:5], -1, 0
	s_and_b64 s[4:5], vcc, s[4:5]
	s_cmp_lt_i32 s95, s76
	s_waitcnt vmcnt(46)
	v_cndmask_b32_e64 v36, 0, v36, s[4:5]
	s_cselect_b64 s[4:5], -1, 0
	s_and_b64 s[4:5], vcc, s[4:5]
	s_cmp_lt_i32 s50, s76
	s_waitcnt vmcnt(45)
	v_cndmask_b32_e64 v35, 0, v35, s[4:5]
	s_cselect_b64 s[4:5], -1, 0
	s_and_b64 s[4:5], vcc, s[4:5]
	s_cmp_lt_i32 s51, s76
	s_waitcnt vmcnt(44)
	v_cndmask_b32_e64 v34, 0, v34, s[4:5]
	s_cselect_b64 s[4:5], -1, 0
	s_and_b64 s[4:5], vcc, s[4:5]
	s_cmp_lt_i32 s52, s76
	s_waitcnt vmcnt(43)
	v_cndmask_b32_e64 v33, 0, v33, s[4:5]
	s_cselect_b64 s[4:5], -1, 0
	s_and_b64 s[4:5], vcc, s[4:5]
	s_cmp_lt_i32 s53, s76
	s_waitcnt vmcnt(42)
	v_cndmask_b32_e64 v32, 0, v32, s[4:5]
	s_cselect_b64 s[4:5], -1, 0
	s_and_b64 s[4:5], vcc, s[4:5]
	s_cmp_lt_i32 s6, s76
	s_waitcnt vmcnt(41)
	v_cndmask_b32_e64 v31, 0, v31, s[4:5]
	s_cselect_b64 s[4:5], -1, 0
	s_and_b64 s[4:5], vcc, s[4:5]
	s_cmp_lt_i32 s7, s76
	s_waitcnt vmcnt(40)
	v_cndmask_b32_e64 v30, 0, v30, s[4:5]
	s_cselect_b64 s[4:5], -1, 0
	s_and_b64 s[4:5], vcc, s[4:5]
	s_cmp_lt_i32 s8, s76
	s_waitcnt vmcnt(39)
	v_cndmask_b32_e64 v45, 0, v45, s[4:5]
	s_cselect_b64 s[4:5], -1, 0
	s_and_b64 s[4:5], vcc, s[4:5]
	s_cmp_lt_i32 s9, s76
	s_waitcnt vmcnt(38)
	v_cndmask_b32_e64 v44, 0, v44, s[4:5]
	s_cselect_b64 s[4:5], -1, 0
	s_and_b64 s[4:5], vcc, s[4:5]
	s_cmp_lt_i32 s10, s76
	s_waitcnt vmcnt(37)
	v_cndmask_b32_e64 v43, 0, v43, s[4:5]
	s_cselect_b64 s[4:5], -1, 0
	s_and_b64 s[4:5], vcc, s[4:5]
	s_cmp_lt_i32 s11, s76
	s_waitcnt vmcnt(36)
	v_cndmask_b32_e64 v42, 0, v42, s[4:5]
	s_cselect_b64 s[4:5], -1, 0
	s_and_b64 s[4:5], vcc, s[4:5]
	s_cmp_lt_i32 s14, s76
	s_waitcnt vmcnt(35)
	v_cndmask_b32_e64 v41, 0, v41, s[4:5]
	s_cselect_b64 s[4:5], -1, 0
	s_and_b64 s[4:5], vcc, s[4:5]
	s_cmp_lt_i32 s15, s76
	s_waitcnt vmcnt(34)
	v_cndmask_b32_e64 v40, 0, v40, s[4:5]
	s_cselect_b64 s[4:5], -1, 0
	s_and_b64 s[4:5], vcc, s[4:5]
	s_cmp_lt_i32 s16, s76
	s_waitcnt vmcnt(33)
	v_cndmask_b32_e64 v39, 0, v39, s[4:5]
	s_cselect_b64 s[4:5], -1, 0
	s_and_b64 s[4:5], vcc, s[4:5]
	s_cmp_lt_i32 s17, s76
	s_waitcnt vmcnt(32)
	v_cndmask_b32_e64 v38, 0, v38, s[4:5]
	s_cselect_b64 s[4:5], -1, 0
	s_and_b64 s[4:5], vcc, s[4:5]
	s_cmp_lt_i32 s12, s76
	s_waitcnt vmcnt(31)
	v_cndmask_b32_e64 v53, 0, v53, s[4:5]
	s_cselect_b64 s[4:5], -1, 0
	s_and_b64 s[4:5], vcc, s[4:5]
	s_cmp_lt_i32 s13, s76
	s_waitcnt vmcnt(30)
	v_cndmask_b32_e64 v52, 0, v52, s[4:5]
	s_cselect_b64 s[4:5], -1, 0
	s_and_b64 s[4:5], vcc, s[4:5]
	s_cmp_lt_i32 s20, s76
	s_waitcnt vmcnt(29)
	v_cndmask_b32_e64 v51, 0, v51, s[4:5]
	s_cselect_b64 s[4:5], -1, 0
	s_and_b64 s[4:5], vcc, s[4:5]
	s_cmp_lt_i32 s21, s76
	s_waitcnt vmcnt(28)
	v_cndmask_b32_e64 v50, 0, v50, s[4:5]
	s_cselect_b64 s[4:5], -1, 0
	s_and_b64 s[4:5], vcc, s[4:5]
	s_cmp_lt_i32 s24, s76
	s_waitcnt vmcnt(27)
	v_cndmask_b32_e64 v49, 0, v49, s[4:5]
	s_cselect_b64 s[4:5], -1, 0
	s_and_b64 s[4:5], vcc, s[4:5]
	s_cmp_lt_i32 s25, s76
	s_waitcnt vmcnt(26)
	v_cndmask_b32_e64 v48, 0, v48, s[4:5]
	s_cselect_b64 s[4:5], -1, 0
	s_and_b64 s[4:5], vcc, s[4:5]
	s_cmp_lt_i32 s26, s76
	s_waitcnt vmcnt(25)
	v_cndmask_b32_e64 v47, 0, v47, s[4:5]
	s_cselect_b64 s[4:5], -1, 0
	s_and_b64 s[4:5], vcc, s[4:5]
	s_cmp_lt_i32 s27, s76
	s_waitcnt vmcnt(24)
; #define LAS __attribute__((address_space(3)))
; #define LDS_WAIT() asm volatile("s_waitcnt lgkmcnt(0)" ::: "memory")
; __device__ __forceinline__ void conv_load(const ConvItem& ci, int lane, float (&v)[64]) {
;     ...
;     for (int i = 0; i < 64; ++i) v[i] = (okc && (ci.k0 + i) < ci.Ksrc) ? v[i] : 0.f;
; }
; __device__ __forceinline__ void conv_store(const ConvItem& ci, LAS float* scr, int lane, const float (&v)[64]) {
;     const int c = lane & 7;
;     f32x4 s0 = {1.f, 1.f, 1.f, 1.f}, s1 = s0;
;     if (ci.ks) { const int kb = ci.k0 + 8 * c < ci.Ksrc - 8 ? ci.k0 + 8 * c : ci.Ksrc - 8; s0 = *(const f32x4*)(ci.ks + kb); s1 = *(const f32x4*)(ci.ks + kb + 4); }
; #pragma unroll
;     for (int i = 0; i < 64; ++i) scr[i * 65 + lane] = v[i];
;     LDS_WAIT(); asm volatile("" ::: "memory");
	v_cndmask_b32_e64 v46, 0, v46, s[4:5]
	s_cselect_b64 s[4:5], -1, 0
	s_and_b64 s[4:5], vcc, s[4:5]
	s_cmp_lt_i32 s18, s76
	s_waitcnt vmcnt(23)
	v_cndmask_b32_e64 v61, 0, v61, s[4:5]
	s_cselect_b64 s[4:5], -1, 0
	s_and_b64 s[4:5], vcc, s[4:5]
	s_cmp_lt_i32 s19, s76
	s_waitcnt vmcnt(22)
	v_cndmask_b32_e64 v60, 0, v60, s[4:5]
	s_cselect_b64 s[4:5], -1, 0
	s_and_b64 s[4:5], vcc, s[4:5]
	s_cmp_lt_i32 s28, s76
	s_waitcnt vmcnt(21)
	v_cndmask_b32_e64 v59, 0, v59, s[4:5]
	s_cselect_b64 s[4:5], -1, 0
	s_and_b64 s[4:5], vcc, s[4:5]
	s_cmp_lt_i32 s29, s76
	s_waitcnt vmcnt(20)
	v_cndmask_b32_e64 v58, 0, v58, s[4:5]
	s_cselect_b64 s[4:5], -1, 0
	s_and_b64 s[4:5], vcc, s[4:5]
	s_cmp_lt_i32 s22, s76
	s_waitcnt vmcnt(19)
	v_cndmask_b32_e64 v57, 0, v57, s[4:5]
	s_cselect_b64 s[4:5], -1, 0
	s_and_b64 s[4:5], vcc, s[4:5]
	s_cmp_lt_i32 s23, s76
	s_waitcnt vmcnt(18)
	v_cndmask_b32_e64 v56, 0, v56, s[4:5]
	s_cselect_b64 s[4:5], -1, 0
	s_and_b64 s[4:5], vcc, s[4:5]
	s_cmp_lt_i32 s30, s76
	s_waitcnt vmcnt(17)
	v_cndmask_b32_e64 v55, 0, v55, s[4:5]
	s_cselect_b64 s[4:5], -1, 0
	s_and_b64 s[4:5], vcc, s[4:5]
	s_cmp_lt_i32 s31, s76
	s_waitcnt vmcnt(16)
	v_cndmask_b32_e64 v54, 0, v54, s[4:5]
	s_cselect_b64 s[4:5], -1, 0
	s_and_b64 s[4:5], vcc, s[4:5]
	s_cmp_lt_i32 s36, s76
	s_waitcnt vmcnt(15)
	v_cndmask_b32_e64 v70, 0, v70, s[4:5]
	s_cselect_b64 s[4:5], -1, 0
	s_and_b64 s[4:5], vcc, s[4:5]
	s_cmp_lt_i32 s37, s76
	s_waitcnt vmcnt(14)
	v_cndmask_b32_e64 v69, 0, v69, s[4:5]
	s_cselect_b64 s[4:5], -1, 0
	s_and_b64 s[4:5], vcc, s[4:5]
	s_cmp_lt_i32 s38, s76
	s_waitcnt vmcnt(13)
	v_cndmask_b32_e64 v68, 0, v68, s[4:5]
	s_cselect_b64 s[4:5], -1, 0
	s_and_b64 s[4:5], vcc, s[4:5]
	s_cmp_lt_i32 s39, s76
	s_waitcnt vmcnt(12)
	v_cndmask_b32_e64 v67, 0, v67, s[4:5]
	s_cselect_b64 s[4:5], -1, 0
	s_and_b64 s[4:5], vcc, s[4:5]
	s_cmp_lt_i32 s34, s76
	s_waitcnt vmcnt(11)
	v_cndmask_b32_e64 v66, 0, v66, s[4:5]
	s_cselect_b64 s[4:5], -1, 0
	s_and_b64 s[4:5], vcc, s[4:5]
	s_cmp_lt_i32 s35, s76
	s_waitcnt vmcnt(10)
	v_cndmask_b32_e64 v64, 0, v64, s[4:5]
	s_cselect_b64 s[4:5], -1, 0
	s_and_b64 s[4:5], vcc, s[4:5]
	s_cmp_lt_i32 s42, s76
	s_waitcnt vmcnt(9)
	v_cndmask_b32_e64 v63, 0, v63, s[4:5]
	s_cselect_b64 s[4:5], -1, 0
	s_and_b64 s[4:5], vcc, s[4:5]
	s_cmp_lt_i32 s43, s76
	s_waitcnt vmcnt(8)
	v_cndmask_b32_e64 v62, 0, v62, s[4:5]
	s_cselect_b64 s[4:5], -1, 0
	s_and_b64 s[4:5], vcc, s[4:5]
	s_cmp_lt_i32 s54, s76
	s_waitcnt vmcnt(7)
	v_cndmask_b32_e64 v65, 0, v65, s[4:5]
	s_cselect_b64 s[4:5], -1, 0
	s_and_b64 s[4:5], vcc, s[4:5]
	s_cmp_lt_i32 s55, s76
	s_waitcnt vmcnt(6)
	v_cndmask_b32_e64 v74, 0, v74, s[4:5]
	s_cselect_b64 s[4:5], -1, 0
	s_and_b64 s[4:5], vcc, s[4:5]
	s_cmp_lt_i32 s46, s76
	ds_write2_b32 v12, v21, v20 offset1:65
	ds_write2_b32 v12, v19, v18 offset0:130 offset1:195
	v_add_u32_e32 v18, 0x400, v12
	s_waitcnt vmcnt(5)
	v_cndmask_b32_e64 v73, 0, v73, s[4:5]
	s_cselect_b64 s[4:5], -1, 0
	ds_write2_b32 v18, v17, v16 offset0:4 offset1:69
	ds_write2_b32 v18, v15, v8 offset0:134 offset1:199
	v_add_u32_e32 v8, 0x800, v12
	s_and_b64 s[4:5], vcc, s[4:5]
	ds_write2_b32 v8, v29, v28 offset0:8 offset1:73
	ds_write2_b32 v8, v27, v26 offset0:138 offset1:203
	v_add_u32_e32 v8, 0xc00, v12
	s_cmp_lt_i32 s47, s76
	ds_write2_b32 v8, v25, v24 offset0:12 offset1:77
	ds_write2_b32 v8, v23, v22 offset0:142 offset1:207
	v_add_u32_e32 v8, 0x1000, v12
	s_waitcnt vmcnt(4)
	v_cndmask_b32_e64 v72, 0, v72, s[4:5]
	s_cselect_b64 s[4:5], -1, 0
	ds_write2_b32 v8, v37, v36 offset0:16 offset1:81
	ds_write2_b32 v8, v35, v34 offset0:146 offset1:211
	v_add_u32_e32 v8, 0x1400, v12
	s_and_b64 s[4:5], vcc, s[4:5]
	ds_write2_b32 v8, v33, v32 offset0:20 offset1:85
	ds_write2_b32 v8, v31, v30 offset0:150 offset1:215
	v_add_u32_e32 v8, 0x1800, v12
	s_cmp_lt_i32 s48, s76
	ds_write2_b32 v8, v45, v44 offset0:24 offset1:89
	ds_write2_b32 v8, v43, v42 offset0:154 offset1:219
	v_add_u32_e32 v8, 0x1c00, v12
	s_waitcnt vmcnt(3)
	v_cndmask_b32_e64 v71, 0, v71, s[4:5]
	s_cselect_b64 s[4:5], -1, 0
	ds_write2_b32 v8, v41, v40 offset0:28 offset1:93
	ds_write2_b32 v8, v39, v38 offset0:158 offset1:223
	v_add_u32_e32 v8, 0x2000, v12
	s_and_b64 s[4:5], vcc, s[4:5]
	ds_write2_b32 v8, v53, v52 offset0:32 offset1:97
	ds_write2_b32 v8, v51, v50 offset0:162 offset1:227
	v_add_u32_e32 v8, 0x2400, v12
	s_cmp_lt_i32 s49, s76
	ds_write2_b32 v8, v49, v48 offset0:36 offset1:101
	ds_write2_b32 v8, v47, v46 offset0:166 offset1:231
	v_add_u32_e32 v8, 0x2800, v12
	s_waitcnt vmcnt(2)
	v_cndmask_b32_e64 v77, 0, v77, s[4:5]
	s_cselect_b64 s[4:5], -1, 0
	ds_write2_b32 v8, v61, v60 offset0:40 offset1:105
	ds_write2_b32 v8, v59, v58 offset0:170 offset1:235
	v_add_u32_e32 v8, 0x2c00, v12
	s_and_b64 s[4:5], vcc, s[4:5]
	ds_write2_b32 v8, v57, v56 offset0:44 offset1:109
	ds_write2_b32 v8, v55, v54 offset0:174 offset1:239
	v_add_u32_e32 v8, 0x3000, v12
	s_cmp_lt_i32 s44, s76
	ds_write2_b32 v8, v70, v69 offset0:48 offset1:113
	ds_write2_b32 v8, v68, v67 offset0:178 offset1:243
	v_add_u32_e32 v8, 0x3400, v12
	s_waitcnt vmcnt(1)
	v_cndmask_b32_e64 v76, 0, v76, s[4:5]
	s_cselect_b64 s[4:5], -1, 0
	ds_write2_b32 v8, v66, v64 offset0:52 offset1:117
	ds_write2_b32 v8, v63, v62 offset0:182 offset1:247
	v_add_u32_e32 v8, 0x3800, v12
	s_and_b64 vcc, vcc, s[4:5]
	ds_write2_b32 v8, v65, v74 offset0:56 offset1:121
	ds_write2_b32 v8, v73, v72 offset0:186 offset1:251
	v_add_u32_e32 v8, 0x3c00, v12
	s_waitcnt vmcnt(0)
	v_cndmask_b32_e32 v75, 0, v75, vcc
	ds_write2_b32 v8, v71, v77 offset0:60 offset1:125
	ds_write2_b32 v8, v76, v75 offset0:190 offset1:255
	s_waitcnt lgkmcnt(0)
; __device__ __forceinline__ unsigned cvt_pk_bf16(float lo, float hi) { unsigned r; asm volatile("v_cvt_pk_bf16_f32 %0, %1, %2" : "=v"(r) : "v"(lo), "v"(hi)); return r; }
; #define LAS __attribute__((address_space(3)))
; #define LDS_WAIT() asm volatile("s_waitcnt lgkmcnt(0)" ::: "memory")
; __device__ __forceinline__ void conv_store(const ConvItem& ci, LAS float* scr, int lane, const float (&v)[64]) {
;     ...
;     LDS_WAIT(); asm volatile("" ::: "memory");
; #pragma unroll
;     for (int j = 0; j < 8; ++j) { const int n = (lane >> 3) + 8 * j; const LAS float* s = scr + (8 * c) * 65 + n;
;         v4u o; o.x = cvt_pk_bf16(s[0 * 65] * s0[0], s[1 * 65] * s0[1]); o.y = cvt_pk_bf16(s[2 * 65] * s0[2], s[3 * 65] * s0[3]); o.z = cvt_pk_bf16(s[4 * 65] * s1[0], s[5 * 65] * s1[1]); o.w = cvt_pk_bf16(s[6 * 65] * s1[2], s[7 * 65] * s1[3]);
;         *(v4u*)(ci.dst + (size_t)(ci.drow0 + n) * ci.ldd + ci.k0 + 8 * c) = o; }
	v_add_u32_e32 v192, 0x400, v14
	ds_read2_b32 v[128:129], v14 offset1:65
	ds_read2_b32 v[130:131], v14 offset0:130 offset1:195
	ds_read2_b32 v[132:133], v192 offset0:4 offset1:69
	ds_read2_b32 v[134:135], v192 offset0:134 offset1:199
	ds_read2_b32 v[136:137], v14 offset0:8 offset1:73
	ds_read2_b32 v[138:139], v14 offset0:138 offset1:203
	ds_read2_b32 v[140:141], v192 offset0:12 offset1:77
	ds_read2_b32 v[142:143], v192 offset0:142 offset1:207
	ds_read2_b32 v[144:145], v14 offset0:16 offset1:81
	ds_read2_b32 v[146:147], v14 offset0:146 offset1:211
	ds_read2_b32 v[148:149], v192 offset0:20 offset1:85
	ds_read2_b32 v[150:151], v192 offset0:150 offset1:215
	ds_read2_b32 v[152:153], v14 offset0:24 offset1:89
	ds_read2_b32 v[154:155], v14 offset0:154 offset1:219
	ds_read2_b32 v[156:157], v192 offset0:28 offset1:93
	ds_read2_b32 v[158:159], v192 offset0:158 offset1:223
	ds_read2_b32 v[160:161], v14 offset0:32 offset1:97
	ds_read2_b32 v[162:163], v14 offset0:162 offset1:227
	ds_read2_b32 v[164:165], v192 offset0:36 offset1:101
	ds_read2_b32 v[166:167], v192 offset0:166 offset1:231
	ds_read2_b32 v[168:169], v14 offset0:40 offset1:105
	ds_read2_b32 v[170:171], v14 offset0:170 offset1:235
	ds_read2_b32 v[172:173], v192 offset0:44 offset1:109
	ds_read2_b32 v[174:175], v192 offset0:174 offset1:239
	ds_read2_b32 v[176:177], v14 offset0:48 offset1:113
	ds_read2_b32 v[178:179], v14 offset0:178 offset1:243
	ds_read2_b32 v[180:181], v192 offset0:52 offset1:117
	ds_read2_b32 v[182:183], v192 offset0:182 offset1:247
	ds_read2_b32 v[184:185], v14 offset0:56 offset1:121
	ds_read2_b32 v[186:187], v14 offset0:186 offset1:251
	ds_read2_b32 v[188:189], v192 offset0:60 offset1:125
	ds_read2_b32 v[190:191], v192 offset0:190 offset1:255
	s_waitcnt lgkmcnt(0)
	v_add_u32_e32 v24, s59, v13
	v_mul_lo_u32 v22, s57, v24
	s_ashr_i32 s59, s58, 31
	v_readlane_b32 s76, v254, 31
	s_waitcnt lgkmcnt(0)
	v_mul_f32_e32 v8, v4, v128
	v_mul_f32_e32 v15, v5, v129
	v_cvt_pk_bf16_f32 v16, v8, v15
	s_add_i32 s3, s3, s33
	s_add_i32 s66, s66, s67
	s_add_i32 s68, s68, s69
	s_add_i32 s70, s70, s71
	s_waitcnt lgkmcnt(0)
	v_mul_f32_e32 v15, v7, v131
	v_mul_f32_e32 v8, v6, v130
	v_cvt_pk_bf16_f32 v17, v8, v15
	v_add_u32_e32 v15, 0x400, v14
	s_add_i32 s72, s72, s73
	s_add_i32 s74, s74, s75
	v_readlane_b32 s78, v254, 33
	v_readlane_b32 s79, v254, 34
	s_waitcnt lgkmcnt(0)
	v_mul_f32_e32 v8, v0, v132
	v_mul_f32_e32 v18, v1, v133
	v_cvt_pk_bf16_f32 v18, v8, v18
	v_readlane_b32 s80, v255, 21
	v_readlane_b32 s77, v254, 32
	s_movk_i32 s78, 0x1580
	v_readlane_b32 s82, v255, 23
	s_waitcnt lgkmcnt(0)
	v_mul_f32_e32 v8, v2, v134
	v_mul_f32_e32 v19, v3, v135
	v_cvt_pk_bf16_f32 v19, v8, v19
	v_ashrrev_i32_e32 v8, 31, v24
	v_mul_lo_u32 v8, s56, v8
	v_mad_u64_u32 v[20:21], s[4:5], s56, v24, 0
	v_add3_u32 v21, v21, v8, v22
	v_lshl_add_u64 v[20:21], v[20:21], 1, s[60:61]
	s_lshl_b64 s[4:5], s[58:59], 1
	v_lshl_add_u64 v[20:21], v[20:21], 0, s[4:5]
	v_lshlrev_b32_e32 v8, 1, v10
	v_lshl_add_u64 v[20:21], v[20:21], 0, v[8:9]
	global_store_dwordx4 v[20:21], v[16:19], off sc1
	s_cmpk_lt_i32 s3, 21440
	v_readlane_b32 s83, v255, 24
	s_waitcnt lgkmcnt(0)
	v_mul_f32_e32 v16, v4, v136
	v_mul_f32_e32 v17, v5, v137
	v_cvt_pk_bf16_f32 v16, v16, v17
	s_mov_b32 s79, 0x3f22f983
	s_mov_b32 s85, 0xbfc90fda
	s_brev_b32 s86, 1
	s_movk_i32 s87, 0x1f8
	s_waitcnt lgkmcnt(0)
	v_mul_f32_e32 v17, v6, v138
	v_mul_f32_e32 v18, v7, v139
	v_cvt_pk_bf16_f32 v17, v17, v18
	s_mov_b64 s[88:89], 0x80
	s_mov_b64 s[92:93], 0x4000
	s_mov_b64 s[94:95], 0x4800
	v_readlane_b32 s81, v255, 22
	s_waitcnt lgkmcnt(0)
	v_mul_f32_e32 v18, v0, v140
	v_mul_f32_e32 v19, v1, v141
	v_cvt_pk_bf16_f32 v18, v18, v19
	s_waitcnt lgkmcnt(0)
	v_mul_f32_e32 v19, v2, v142
	v_mul_f32_e32 v20, v3, v143
	v_cvt_pk_bf16_f32 v19, v19, v20
	v_add_u32_e32 v20, 8, v24
	v_ashrrev_i32_e32 v21, 31, v20
	v_mul_lo_u32 v22, s56, v21
	v_mul_lo_u32 v23, s57, v20
	v_mad_u64_u32 v[20:21], s[6:7], s56, v20, 0
	v_add3_u32 v21, v21, v22, v23
	v_lshl_add_u64 v[20:21], v[20:21], 1, s[60:61]
	v_lshl_add_u64 v[20:21], v[20:21], 0, s[4:5]
	v_lshl_add_u64 v[20:21], v[20:21], 0, v[8:9]
	global_store_dwordx4 v[20:21], v[16:19], off sc1
	s_waitcnt lgkmcnt(0)
	s_nop 0
	v_mul_f32_e32 v16, v4, v144
	v_mul_f32_e32 v17, v5, v145
	v_cvt_pk_bf16_f32 v16, v16, v17
	s_waitcnt lgkmcnt(0)
	v_mul_f32_e32 v17, v6, v146
	v_mul_f32_e32 v18, v7, v147
	v_cvt_pk_bf16_f32 v17, v17, v18
	s_waitcnt lgkmcnt(0)
	v_mul_f32_e32 v18, v0, v148
	v_mul_f32_e32 v19, v1, v149
	v_cvt_pk_bf16_f32 v18, v18, v19
	s_waitcnt lgkmcnt(0)
; __device__ __forceinline__ unsigned cvt_pk_bf16(float lo, float hi) { unsigned r; asm volatile("v_cvt_pk_bf16_f32 %0, %1, %2" : "=v"(r) : "v"(lo), "v"(hi)); return r; }
; #define LAS __attribute__((address_space(3)))
; __device__ __forceinline__ void conv_store(const ConvItem& ci, LAS float* scr, int lane, const float (&v)[64]) {
;     ...
;     for (int j = 0; j < 8; ++j) { const int n = (lane >> 3) + 8 * j; const LAS float* s = scr + (8 * c) * 65 + n;
;         v4u o; o.x = cvt_pk_bf16(s[0 * 65] * s0[0], s[1 * 65] * s0[1]); o.y = cvt_pk_bf16(s[2 * 65] * s0[2], s[3 * 65] * s0[3]); o.z = cvt_pk_bf16(s[4 * 65] * s1[0], s[5 * 65] * s1[1]); o.w = cvt_pk_bf16(s[6 * 65] * s1[2], s[7 * 65] * s1[3]);
;         *(v4u*)(ci.dst + (size_t)(ci.drow0 + n) * ci.ldd + ci.k0 + 8 * c) = o; }
	v_mul_f32_e32 v19, v2, v150
	v_mul_f32_e32 v20, v3, v151
	v_cvt_pk_bf16_f32 v19, v19, v20
	v_add_u32_e32 v20, 16, v24
	v_ashrrev_i32_e32 v21, 31, v20
	v_mul_lo_u32 v22, s56, v21
	v_mul_lo_u32 v23, s57, v20
	v_mad_u64_u32 v[20:21], s[6:7], s56, v20, 0
	v_add3_u32 v21, v21, v22, v23
	v_lshl_add_u64 v[20:21], v[20:21], 1, s[60:61]
	v_lshl_add_u64 v[20:21], v[20:21], 0, s[4:5]
	v_lshl_add_u64 v[20:21], v[20:21], 0, v[8:9]
	global_store_dwordx4 v[20:21], v[16:19], off sc1
	s_waitcnt lgkmcnt(0)
	s_nop 0
	v_mul_f32_e32 v16, v4, v152
	v_mul_f32_e32 v17, v5, v153
	v_cvt_pk_bf16_f32 v16, v16, v17
	s_waitcnt lgkmcnt(0)
	v_mul_f32_e32 v17, v6, v154
	v_mul_f32_e32 v18, v7, v155
	v_cvt_pk_bf16_f32 v17, v17, v18
	s_waitcnt lgkmcnt(0)
	v_mul_f32_e32 v18, v0, v156
	v_mul_f32_e32 v19, v1, v157
	v_cvt_pk_bf16_f32 v18, v18, v19
	s_waitcnt lgkmcnt(0)
	v_mul_f32_e32 v19, v2, v158
	v_mul_f32_e32 v20, v3, v159
	v_cvt_pk_bf16_f32 v19, v19, v20
	v_add_u32_e32 v20, 24, v24
	v_ashrrev_i32_e32 v21, 31, v20
	v_mul_lo_u32 v22, s56, v21
	v_mul_lo_u32 v23, s57, v20
	v_mad_u64_u32 v[20:21], s[6:7], s56, v20, 0
	v_add3_u32 v21, v21, v22, v23
	v_lshl_add_u64 v[20:21], v[20:21], 1, s[60:61]
	v_lshl_add_u64 v[20:21], v[20:21], 0, s[4:5]
	v_lshl_add_u64 v[20:21], v[20:21], 0, v[8:9]
	global_store_dwordx4 v[20:21], v[16:19], off sc1
	s_waitcnt lgkmcnt(0)
	s_nop 0
	v_mul_f32_e32 v16, v4, v160
	v_mul_f32_e32 v17, v5, v161
	v_cvt_pk_bf16_f32 v16, v16, v17
	s_waitcnt lgkmcnt(0)
	v_mul_f32_e32 v17, v6, v162
	v_mul_f32_e32 v18, v7, v163
	v_cvt_pk_bf16_f32 v17, v17, v18
	s_waitcnt lgkmcnt(0)
	v_mul_f32_e32 v18, v0, v164
	v_mul_f32_e32 v19, v1, v165
	v_cvt_pk_bf16_f32 v18, v18, v19
	s_waitcnt lgkmcnt(0)
	v_mul_f32_e32 v19, v2, v166
	v_mul_f32_e32 v20, v3, v167
	v_cvt_pk_bf16_f32 v19, v19, v20
	v_add_u32_e32 v20, 32, v24
	v_ashrrev_i32_e32 v21, 31, v20
	v_mul_lo_u32 v22, s56, v21
	v_mul_lo_u32 v23, s57, v20
	v_mad_u64_u32 v[20:21], s[6:7], s56, v20, 0
	v_add3_u32 v21, v21, v22, v23
	v_lshl_add_u64 v[20:21], v[20:21], 1, s[60:61]
	v_lshl_add_u64 v[20:21], v[20:21], 0, s[4:5]
	v_lshl_add_u64 v[20:21], v[20:21], 0, v[8:9]
	global_store_dwordx4 v[20:21], v[16:19], off sc1
	s_waitcnt lgkmcnt(0)
	s_nop 0
	v_mul_f32_e32 v16, v4, v168
	v_mul_f32_e32 v17, v5, v169
	v_cvt_pk_bf16_f32 v16, v16, v17
	s_waitcnt lgkmcnt(0)
	v_mul_f32_e32 v17, v6, v170
	v_mul_f32_e32 v18, v7, v171
	v_cvt_pk_bf16_f32 v17, v17, v18
	s_waitcnt lgkmcnt(0)
	v_mul_f32_e32 v18, v0, v172
	v_mul_f32_e32 v19, v1, v173
	v_cvt_pk_bf16_f32 v18, v18, v19
	s_waitcnt lgkmcnt(0)
	v_mul_f32_e32 v19, v2, v174
	v_mul_f32_e32 v20, v3, v175
	v_cvt_pk_bf16_f32 v19, v19, v20
	v_add_u32_e32 v20, 40, v24
	v_ashrrev_i32_e32 v21, 31, v20
	v_mul_lo_u32 v22, s56, v21
	v_mul_lo_u32 v23, s57, v20
	v_mad_u64_u32 v[20:21], s[6:7], s56, v20, 0
	v_add3_u32 v21, v21, v22, v23
	v_lshl_add_u64 v[20:21], v[20:21], 1, s[60:61]
	v_lshl_add_u64 v[20:21], v[20:21], 0, s[4:5]
	v_lshl_add_u64 v[20:21], v[20:21], 0, v[8:9]
	global_store_dwordx4 v[20:21], v[16:19], off sc1
	s_waitcnt lgkmcnt(0)
	s_nop 0
	v_mul_f32_e32 v16, v4, v176
	v_mul_f32_e32 v17, v5, v177
	v_cvt_pk_bf16_f32 v16, v16, v17
	s_waitcnt lgkmcnt(0)
	v_mul_f32_e32 v17, v6, v178
	v_mul_f32_e32 v18, v7, v179
	v_cvt_pk_bf16_f32 v17, v17, v18
	s_waitcnt lgkmcnt(0)
	v_mul_f32_e32 v18, v0, v180
	v_mul_f32_e32 v19, v1, v181
	v_cvt_pk_bf16_f32 v18, v18, v19
	s_waitcnt lgkmcnt(0)
	v_mul_f32_e32 v19, v2, v182
	v_mul_f32_e32 v20, v3, v183
	v_cvt_pk_bf16_f32 v19, v19, v20
	v_add_u32_e32 v20, 48, v24
	v_ashrrev_i32_e32 v21, 31, v20
	v_mul_lo_u32 v22, s56, v21
	v_mul_lo_u32 v23, s57, v20
	v_mad_u64_u32 v[20:21], s[6:7], s56, v20, 0
	v_add3_u32 v21, v21, v22, v23
	v_lshl_add_u64 v[20:21], v[20:21], 1, s[60:61]
	v_lshl_add_u64 v[20:21], v[20:21], 0, s[4:5]
	v_lshl_add_u64 v[20:21], v[20:21], 0, v[8:9]
	global_store_dwordx4 v[20:21], v[16:19], off sc1
	s_waitcnt lgkmcnt(0)
	v_mul_f32_e32 v4, v4, v184
	v_mul_f32_e32 v5, v5, v185
	v_cvt_pk_bf16_f32 v4, v4, v5
	s_waitcnt lgkmcnt(0)
	v_mul_f32_e32 v5, v6, v186
	v_mul_f32_e32 v6, v7, v187
	v_cvt_pk_bf16_f32 v5, v5, v6
	s_waitcnt lgkmcnt(0)
	v_mul_f32_e32 v0, v0, v188
	v_mul_f32_e32 v1, v1, v189
	v_cvt_pk_bf16_f32 v6, v0, v1
	s_waitcnt lgkmcnt(0)
	v_mul_f32_e32 v0, v2, v190
	v_mul_f32_e32 v1, v3, v191
	v_cvt_pk_bf16_f32 v7, v0, v1
	v_add_u32_e32 v0, 56, v24
	v_ashrrev_i32_e32 v1, 31, v0
	v_mul_lo_u32 v2, s56, v1
	v_mul_lo_u32 v3, s57, v0
	v_mad_u64_u32 v[0:1], s[6:7], s56, v0, 0
	v_add3_u32 v1, v1, v2, v3
	v_lshl_add_u64 v[0:1], v[0:1], 1, s[60:61]
	v_lshl_add_u64 v[0:1], v[0:1], 0, s[4:5]
	v_lshl_add_u64 v[0:1], v[0:1], 0, v[8:9]
	global_store_dwordx4 v[0:1], v[4:7], off sc1
	s_waitcnt lgkmcnt(0)
	s_cbranch_scc0 .Lcvp0c_ret
